# nt hint also on the write-once stores of the hosted weight-conversion loops (outputs are not re-read before a later phase)
# baseline (speedup 1.0000x reference)
; #define GAS __attribute__((address_space(1)))
; __device__ __forceinline__ void conv8_store(const ConvJob& J, int tid, const f32x4 (&v)[16]) {
;     const int nblk = J.ncols / 256, k0 = 128 * (J.item / nblk), n0 = J.ncol0 + 256 * (J.item % nblk);
;     const int lane = tid & 63, w = tid >> 6, kg = lane & 7, nq = lane >> 3; const float sc8 = J.sc8;
; #pragma unroll
;     for (int c = 0; c < 4; ++c) { u32x4 o;
; #pragma unroll
;         for (int d = 0; d < 4; ++d) { int wv = __builtin_amdgcn_cvt_pk_fp8_f32(v[4 * d][c] * sc8, v[4 * d + 1][c] * sc8, 0, false);
;             wv = __builtin_amdgcn_cvt_pk_fp8_f32(v[4 * d + 2][c] * sc8, v[4 * d + 3][c] * sc8, wv, true); o[d] = (unsigned)wv; }
;         *(GAS u32x4*)(J.WT + (size_t)conv_dst_row(J.mode, n0 - J.ncol0 + 32 * w + 4 * nq + c) * J.K + k0 + 16 * kg) = o; }
;     ...
;                 const int q1 = q + F.G; const bool m1 = q1 < q_hi;
;                 if (m1) conv8_load(decode(q1 < I_IN ? q1 : q1 + NB16), tid, vb);
;                 conv8_store(decode(q < I_IN ? q : q + NB16), tid, va);
;                 if (!m1) break;
.LBB0_402:
	v_mul_f32_e32 v141, s24, v49
	v_mul_f32_e32 v144, s24, v53
	v_mov_b32_e32 v140, v163
	v_cvt_pk_fp8_f32 v140, v141, v144
	v_mul_f32_e32 v144, s24, v77
	v_mul_f32_e32 v145, s24, v85
	v_mov_b32_e32 v141, v163
	v_cvt_pk_fp8_f32 v141, v144, v145
	v_mul_f32_e32 v142, s24, v61
	v_mul_f32_e32 v143, s24, v69
	v_cvt_pk_fp8_f32 v140, v142, v143 op_sel:[0,0,1]
	v_mul_f32_e32 v142, s24, v89
	v_mul_f32_e32 v143, s24, v97
	v_cvt_pk_fp8_f32 v141, v142, v143 op_sel:[0,0,1]
	v_mul_f32_e32 v143, s24, v101
	v_mul_f32_e32 v146, s24, v105
	v_mov_b32_e32 v142, v163
	v_cvt_pk_fp8_f32 v142, v143, v146
	v_mul_f32_e32 v146, s24, v117
	v_mul_f32_e32 v147, s24, v121
	v_mov_b32_e32 v143, v163
	v_cvt_pk_fp8_f32 v143, v146, v147
	v_mul_f32_e32 v144, s24, v109
	v_mul_f32_e32 v145, s24, v113
	v_cvt_pk_fp8_f32 v142, v144, v145 op_sel:[0,0,1]
	v_mul_f32_e32 v144, s24, v125
	v_mul_f32_e32 v145, s24, v129
	v_cvt_pk_fp8_f32 v143, v144, v145 op_sel:[0,0,1]
	v_ashrrev_i32_e32 v146, 31, v139
	v_mov_b64_e32 v[144:145], s[80:81]
	v_mad_u64_u32 v[144:145], s[24:25], s78, v139, v[144:145]
	v_mul_lo_u32 v139, s79, v139
	v_mul_lo_u32 v146, s78, v146
	s_add_i32 s1, s0, s30
	v_add3_u32 v145, v139, v145, v146
	v_lshl_add_u64 v[144:145], v[144:145], 0, s[82:83]
	s_cmpk_gt_i32 s1, 0x13ff
	v_lshl_add_u64 v[144:145], v[144:145], 0, v[130:131]
	s_cselect_b64 s[78:79], -1, 0
	global_store_dwordx4 v[144:145], v[140:143], off nt

; #define GAS __attribute__((address_space(1)))
; __device__ __forceinline__ int conv_dst_row(int mode, int n) {
;     if (mode == 1) { if (n >= C_AQ && n < C_AV) { const int hb = n & ~127, dd = n & 127; return hb + (dd < 64 ? 2 * dd : 2 * (dd - 64) + 1); } return n; }
;     if (mode == 2) return (n >> 7) * 256 + (n & 127);
;     if (mode == 3) return (n >> 7) * 256 + 128 + (n & 127);
;     return n;
; }
; __device__ __forceinline__ void conv8_store(const ConvJob& J, int tid, const f32x4 (&v)[16]) {
;     const int nblk = J.ncols / 256, k0 = 128 * (J.item / nblk), n0 = J.ncol0 + 256 * (J.item % nblk);
;     const int lane = tid & 63, w = tid >> 6, kg = lane & 7, nq = lane >> 3; const float sc8 = J.sc8;
; #pragma unroll
;     for (int c = 0; c < 4; ++c) { u32x4 o;
; #pragma unroll
;         for (int d = 0; d < 4; ++d) { int wv = __builtin_amdgcn_cvt_pk_fp8_f32(v[4 * d][c] * sc8, v[4 * d + 1][c] * sc8, 0, false);
;             wv = __builtin_amdgcn_cvt_pk_fp8_f32(v[4 * d + 2][c] * sc8, v[4 * d + 3][c] * sc8, wv, true); o[d] = (unsigned)wv; }
;         *(GAS u32x4*)(J.WT + (size_t)conv_dst_row(J.mode, n0 - J.ncol0 + 32 * w + 4 * nq + c) * J.K + k0 + 16 * kg) = o; }
.LBB0_468:
	s_waitcnt vmcnt(0)
	v_mul_f32_e32 v141, s25, v2
	v_mul_f32_e32 v143, s25, v6
	v_mov_b32_e32 v142, v163
	v_cvt_pk_fp8_f32 v142, v141, v143
	v_mul_f32_e32 v145, s25, v18
	v_mul_f32_e32 v146, s25, v22
	v_mov_b32_e32 v143, v163
	v_cvt_pk_fp8_f32 v143, v145, v146
	v_mul_f32_e32 v141, s25, v10
	v_mul_f32_e32 v144, s25, v14
	v_cvt_pk_fp8_f32 v142, v141, v144 op_sel:[0,0,1]
	v_mul_f32_e32 v141, s25, v26
	v_mul_f32_e32 v144, s25, v30
	v_cvt_pk_fp8_f32 v143, v141, v144 op_sel:[0,0,1]
	v_mul_f32_e32 v141, s25, v34
	v_mul_f32_e32 v145, s25, v38
	v_mov_b32_e32 v144, v163
	v_cvt_pk_fp8_f32 v144, v141, v145
	v_mul_f32_e32 v147, s25, v62
	v_mul_f32_e32 v148, s25, v70
	v_mov_b32_e32 v145, v163
	v_cvt_pk_fp8_f32 v145, v147, v148
	v_mul_f32_e32 v141, s25, v42
	v_mul_f32_e32 v146, s25, v54
	v_cvt_pk_fp8_f32 v144, v141, v146 op_sel:[0,0,1]
	v_mul_f32_e32 v141, s25, v78
	v_mul_f32_e32 v146, s25, v90
	s_add_i32 s50, s50, s33
	v_cvt_pk_fp8_f32 v145, v141, v146 op_sel:[0,0,1]
	v_ashrrev_i32_e32 v141, 31, v140
	v_mov_b64_e32 v[146:147], s[82:83]
	v_add_u32_e32 v139, s50, v135
	s_lshl_b32 s84, s58, 7
	v_mad_u64_u32 v[146:147], s[50:51], s80, v140, v[146:147]
	v_mul_lo_u32 v140, s81, v140
	v_mul_lo_u32 v141, s80, v141
	s_ashr_i32 s85, s84, 31
	v_add3_u32 v147, v140, v147, v141
	v_lshl_add_u64 v[140:141], v[146:147], 0, s[84:85]
	v_lshl_add_u64 v[140:141], v[140:141], 0, v[130:131]
	global_store_dwordx4 v[140:141], v[142:145], off nt
	s_cmp_lt_i32 s24, 2
	s_mov_b64 s[86:87], -1
	v_or_b32_e32 v142, 1, v139
	v_subrev_u32_e32 v141, s33, v142
	s_cbranch_scc1 .LBB0_474
	s_cmp_gt_i32 s24, 2
	v_lshlrev_b32_e32 v143, 1, v141
	s_cbranch_scc0 .LBB0_471
	v_and_b32_e32 v140, 0xffffff00, v143
	v_and_b32_e32 v144, 0x7d, v142
	v_or3_b32 v140, v144, v140, s2
	s_mov_b64 s[86:87], 0

; #define GAS __attribute__((address_space(1)))
; __device__ __forceinline__ int conv_dst_row(int mode, int n) {
;     if (mode == 1) { if (n >= C_AQ && n < C_AV) { const int hb = n & ~127, dd = n & 127; return hb + (dd < 64 ? 2 * dd : 2 * (dd - 64) + 1); } return n; }
;     if (mode == 2) return (n >> 7) * 256 + (n & 127);
;     if (mode == 3) return (n >> 7) * 256 + 128 + (n & 127);
;     return n;
; }
; __device__ __forceinline__ void conv8_store(const ConvJob& J, int tid, const f32x4 (&v)[16]) {
;     const int nblk = J.ncols / 256, k0 = 128 * (J.item / nblk), n0 = J.ncol0 + 256 * (J.item % nblk);
;     const int lane = tid & 63, w = tid >> 6, kg = lane & 7, nq = lane >> 3; const float sc8 = J.sc8;
; #pragma unroll
;     for (int c = 0; c < 4; ++c) { u32x4 o;
; #pragma unroll
;         for (int d = 0; d < 4; ++d) { int wv = __builtin_amdgcn_cvt_pk_fp8_f32(v[4 * d][c] * sc8, v[4 * d + 1][c] * sc8, 0, false);
;             wv = __builtin_amdgcn_cvt_pk_fp8_f32(v[4 * d + 2][c] * sc8, v[4 * d + 3][c] * sc8, wv, true); o[d] = (unsigned)wv; }
;         *(GAS u32x4*)(J.WT + (size_t)conv_dst_row(J.mode, n0 - J.ncol0 + 32 * w + 4 * nq + c) * J.K + k0 + 16 * kg) = o; }
.LBB0_478:
	v_mul_f32_e32 v141, s25, v3
	v_mul_f32_e32 v143, s25, v7
	v_mov_b32_e32 v142, v163
	v_cvt_pk_fp8_f32 v142, v141, v143
	v_mul_f32_e32 v145, s25, v19
	v_mul_f32_e32 v146, s25, v23
	v_mov_b32_e32 v143, v163
	v_cvt_pk_fp8_f32 v143, v145, v146
	v_mul_f32_e32 v141, s25, v11
	v_mul_f32_e32 v144, s25, v15
	v_cvt_pk_fp8_f32 v142, v141, v144 op_sel:[0,0,1]
	v_mul_f32_e32 v141, s25, v27
	v_mul_f32_e32 v144, s25, v31
	v_cvt_pk_fp8_f32 v143, v141, v144 op_sel:[0,0,1]
	v_mul_f32_e32 v141, s25, v35
	v_mul_f32_e32 v145, s25, v39
	v_mov_b32_e32 v144, v163
	v_cvt_pk_fp8_f32 v144, v141, v145
	v_mul_f32_e32 v147, s25, v63
	v_mul_f32_e32 v148, s25, v71
	v_mov_b32_e32 v145, v163
	v_cvt_pk_fp8_f32 v145, v147, v148
	v_mul_f32_e32 v141, s25, v43
	v_mul_f32_e32 v146, s25, v55
	v_cvt_pk_fp8_f32 v144, v141, v146 op_sel:[0,0,1]
	v_mul_f32_e32 v141, s25, v79
	v_mul_f32_e32 v146, s25, v91
	v_cvt_pk_fp8_f32 v145, v141, v146 op_sel:[0,0,1]
	v_ashrrev_i32_e32 v141, 31, v140
	v_mov_b64_e32 v[146:147], s[82:83]
	v_mad_u64_u32 v[146:147], s[50:51], s80, v140, v[146:147]
	v_mul_lo_u32 v140, s81, v140
	v_mul_lo_u32 v141, s80, v141
	v_add3_u32 v147, v140, v147, v141
	v_lshl_add_u64 v[140:141], v[146:147], 0, s[84:85]
	v_lshl_add_u64 v[140:141], v[140:141], 0, v[130:131]
	global_store_dwordx4 v[140:141], v[142:145], off nt
	s_cmp_lt_i32 s24, 2
	s_mov_b64 s[86:87], -1
	v_or_b32_e32 v142, 2, v139
	v_subrev_u32_e32 v141, s33, v142
	s_cbranch_scc1 .LBB0_484
	s_cmp_gt_i32 s24, 2
	v_lshlrev_b32_e32 v143, 1, v141
	s_cbranch_scc0 .LBB0_481
	v_and_b32_e32 v140, 0xffffff00, v143
	v_and_b32_e32 v144, 0x7e, v142
	v_or3_b32 v140, v144, v140, s2
	s_mov_b64 s[86:87], 0

; #define GAS __attribute__((address_space(1)))
; __device__ __forceinline__ int conv_dst_row(int mode, int n) {
;     if (mode == 1) { if (n >= C_AQ && n < C_AV) { const int hb = n & ~127, dd = n & 127; return hb + (dd < 64 ? 2 * dd : 2 * (dd - 64) + 1); } return n; }
;     if (mode == 2) return (n >> 7) * 256 + (n & 127);
;     if (mode == 3) return (n >> 7) * 256 + 128 + (n & 127);
;     return n;
; }
; __device__ __forceinline__ void conv8_store(const ConvJob& J, int tid, const f32x4 (&v)[16]) {
;     const int nblk = J.ncols / 256, k0 = 128 * (J.item / nblk), n0 = J.ncol0 + 256 * (J.item % nblk);
;     const int lane = tid & 63, w = tid >> 6, kg = lane & 7, nq = lane >> 3; const float sc8 = J.sc8;
; #pragma unroll
;     for (int c = 0; c < 4; ++c) { u32x4 o;
; #pragma unroll
;         for (int d = 0; d < 4; ++d) { int wv = __builtin_amdgcn_cvt_pk_fp8_f32(v[4 * d][c] * sc8, v[4 * d + 1][c] * sc8, 0, false);
;             wv = __builtin_amdgcn_cvt_pk_fp8_f32(v[4 * d + 2][c] * sc8, v[4 * d + 3][c] * sc8, wv, true); o[d] = (unsigned)wv; }
;         *(GAS u32x4*)(J.WT + (size_t)conv_dst_row(J.mode, n0 - J.ncol0 + 32 * w + 4 * nq + c) * J.K + k0 + 16 * kg) = o; }
.LBB0_488:
	v_mul_f32_e32 v141, s25, v4
	v_mul_f32_e32 v143, s25, v8
	v_mov_b32_e32 v142, v163
	v_cvt_pk_fp8_f32 v142, v141, v143
	v_mul_f32_e32 v145, s25, v20
	v_mul_f32_e32 v146, s25, v24
	v_mov_b32_e32 v143, v163
	v_cvt_pk_fp8_f32 v143, v145, v146
	v_mul_f32_e32 v141, s25, v12
	v_mul_f32_e32 v144, s25, v16
	v_cvt_pk_fp8_f32 v142, v141, v144 op_sel:[0,0,1]
	v_mul_f32_e32 v141, s25, v28
	v_mul_f32_e32 v144, s25, v32
	v_cvt_pk_fp8_f32 v143, v141, v144 op_sel:[0,0,1]
	v_mul_f32_e32 v141, s25, v36
	v_mul_f32_e32 v145, s25, v40
	v_mov_b32_e32 v144, v163
	v_cvt_pk_fp8_f32 v144, v141, v145
	v_mul_f32_e32 v147, s25, v64
	v_mul_f32_e32 v148, s25, v72
	v_mov_b32_e32 v145, v163
	v_cvt_pk_fp8_f32 v145, v147, v148
	v_mul_f32_e32 v141, s25, v44
	v_mul_f32_e32 v146, s25, v56
	v_cvt_pk_fp8_f32 v144, v141, v146 op_sel:[0,0,1]
	v_mul_f32_e32 v141, s25, v80
	v_mul_f32_e32 v146, s25, v92
	v_cvt_pk_fp8_f32 v145, v141, v146 op_sel:[0,0,1]
	v_ashrrev_i32_e32 v141, 31, v140
	v_mov_b64_e32 v[146:147], s[82:83]
	v_mad_u64_u32 v[146:147], s[50:51], s80, v140, v[146:147]
	v_mul_lo_u32 v140, s81, v140
	v_mul_lo_u32 v141, s80, v141
	v_add3_u32 v147, v140, v147, v141
	v_lshl_add_u64 v[140:141], v[146:147], 0, s[84:85]
	v_lshl_add_u64 v[140:141], v[140:141], 0, v[130:131]
	global_store_dwordx4 v[140:141], v[142:145], off nt
	v_or_b32_e32 v141, 3, v139
	v_subrev_u32_e32 v140, s33, v141
	s_cmp_lt_i32 s24, 2
	s_mov_b64 s[86:87], -1
	s_cbranch_scc1 .LBB0_494
	s_cmp_gt_i32 s24, 2
	v_lshlrev_b32_e32 v142, 1, v140
	s_cbranch_scc0 .LBB0_491
	v_and_b32_e32 v139, 0xffffff00, v142
	v_and_b32_e32 v143, 0x7f, v141
	v_or3_b32 v139, v143, v139, s2
	s_mov_b64 s[86:87], 0

; #define GAS __attribute__((address_space(1)))
; __device__ __forceinline__ void conv8_store(const ConvJob& J, int tid, const f32x4 (&v)[16]) {
;     const int nblk = J.ncols / 256, k0 = 128 * (J.item / nblk), n0 = J.ncol0 + 256 * (J.item % nblk);
;     const int lane = tid & 63, w = tid >> 6, kg = lane & 7, nq = lane >> 3; const float sc8 = J.sc8;
; #pragma unroll
;     for (int c = 0; c < 4; ++c) { u32x4 o;
; #pragma unroll
;         for (int d = 0; d < 4; ++d) { int wv = __builtin_amdgcn_cvt_pk_fp8_f32(v[4 * d][c] * sc8, v[4 * d + 1][c] * sc8, 0, false);
;             wv = __builtin_amdgcn_cvt_pk_fp8_f32(v[4 * d + 2][c] * sc8, v[4 * d + 3][c] * sc8, wv, true); o[d] = (unsigned)wv; }
;         *(GAS u32x4*)(J.WT + (size_t)conv_dst_row(J.mode, n0 - J.ncol0 + 32 * w + 4 * nq + c) * J.K + k0 + 16 * kg) = o; }
;     ...
;     auto decode = [&](int it) -> ConvJob {
;         int r = it;
;         if (r < I_IN) return ConvJob{w_in, ws + WS_WIN, D_MODEL, IN_WIDTH, 1, r, 0, IN_WIDTH, 1, 64.f}; r -= I_IN;
;         if (r < I_INF) return ConvJob{w_in, ws + WS_WINF, D_MODEL, IN_WIDTH, 0, r, C_HF, HG_WIDTH, 0, 1.f}; r -= I_INF;
;         if (r < I_HG) return ConvJob{w_hg, ws + WS_WHG, HG_WIDTH, D_MODEL, 0, r, 0, D_MODEL, 0, 1.f}; r -= I_HG;
;         if (r < I_ATT) return ConvJob{w_att, ws + WS_WATT, ATT_OUT, D_MODEL, 0, r, 0, D_MODEL, 0, 1.f}; r -= I_ATT;
;         if (r < I_OUT) return ConvJob{w_out, ws + WS_WOUT, D_MODEL, D_MODEL, 0, r, 0, D_MODEL, 1, 64.f}; r -= I_OUT;
;         const int which = r / (NEXP1 * I_E); r -= which * (NEXP1 * I_E);
;         const int e = r / I_E, ri = r % I_E; const int es = gu8 ? 1 : 2;
;         if (which == 0) return ConvJob{(e < N_EXPERTS) ? w_eg + (size_t)e * D_MODEL * EXPERT_FF : w_sg, ws + (moe8 ? WS_WGU8 : WS_WGU) + (size_t)e * 1024 * D_MODEL * es, D_MODEL, EXPERT_FF, 2, ri, 0, EXPERT_FF, gu8 ? 1 : 0, 64.f};
;         if (which == 1) return ConvJob{(e < N_EXPERTS) ? w_eu + (size_t)e * D_MODEL * EXPERT_FF : w_su, ws + (moe8 ? WS_WGU8 : WS_WGU) + (size_t)e * 1024 * D_MODEL * es, D_MODEL, EXPERT_FF, 3, ri, 0, EXPERT_FF, gu8 ? 1 : 0, 64.f};
;         return ConvJob{(e < N_EXPERTS) ? w_ed + (size_t)e * EXPERT_FF * D_MODEL : w_sd, ws + (moe8 ? WS_WDN8 : WS_WDN) + (size_t)e * D_MODEL * EXPERT_FF, EXPERT_FF, D_MODEL, 0, ri, 0, D_MODEL, 1, 64.f};
.LBB0_498:
	v_mul_f32_e32 v141, s25, v5
	v_mul_f32_e32 v144, s25, v9
	v_mov_b32_e32 v140, v163
	v_cvt_pk_fp8_f32 v140, v141, v144
	v_mul_f32_e32 v144, s25, v21
	v_mul_f32_e32 v145, s25, v25
	v_mov_b32_e32 v141, v163
	v_cvt_pk_fp8_f32 v141, v144, v145
	v_mul_f32_e32 v142, s25, v13
	v_mul_f32_e32 v143, s25, v17
	v_cvt_pk_fp8_f32 v140, v142, v143 op_sel:[0,0,1]
	v_mul_f32_e32 v142, s25, v29
	v_mul_f32_e32 v143, s25, v33
	v_cvt_pk_fp8_f32 v141, v142, v143 op_sel:[0,0,1]
	v_mul_f32_e32 v143, s25, v37
	v_mul_f32_e32 v146, s25, v41
	v_mov_b32_e32 v142, v163
	v_cvt_pk_fp8_f32 v142, v143, v146
	v_mul_f32_e32 v146, s25, v65
	v_mul_f32_e32 v147, s25, v73
	v_mov_b32_e32 v143, v163
	v_cvt_pk_fp8_f32 v143, v146, v147
	v_mul_f32_e32 v144, s25, v45
	v_mul_f32_e32 v145, s25, v57
	v_cvt_pk_fp8_f32 v142, v144, v145 op_sel:[0,0,1]
	v_mul_f32_e32 v144, s25, v81
	v_mul_f32_e32 v145, s25, v93
	v_cvt_pk_fp8_f32 v143, v144, v145 op_sel:[0,0,1]
	v_ashrrev_i32_e32 v146, 31, v139
	v_mov_b64_e32 v[144:145], s[82:83]
	v_mad_u64_u32 v[144:145], s[24:25], s80, v139, v[144:145]
	v_mul_lo_u32 v139, s81, v139
	v_mul_lo_u32 v146, s80, v146
	v_add3_u32 v145, v139, v145, v146
	v_lshl_add_u64 v[144:145], v[144:145], 0, s[84:85]
	v_lshl_add_u64 v[144:145], v[144:145], 0, v[130:131]
	s_andn2_b64 vcc, exec, s[78:79]
	s_mov_b64 s[78:79], -1
	global_store_dwordx4 v[144:145], v[140:143], off nt
	s_cbranch_vccnz .LBB0_403
	s_add_i32 s1, s64, s1
	s_cmpk_gt_i32 s1, 0x13ff
	s_cbranch_scc1 .LBB0_528
	s_add_i32 s24, s1, 0xa0
	s_cmpk_lt_i32 s1, 0x320
	s_cselect_b32 s1, s1, s24
	s_cmpk_lt_i32 s1, 0x320
	s_cbranch_scc1 .LBB0_513
	s_cmpk_gt_u32 s1, 0x35f
	s_cbranch_scc0 .LBB0_514
	s_cmpk_gt_u32 s1, 0x39f
	s_cbranch_scc0 .LBB0_515
	s_cmpk_gt_u32 s1, 0x3bf
	s_cbranch_scc0 .LBB0_516
	s_cmpk_gt_u32 s1, 0x43f
	s_cbranch_scc0 .LBB0_518
	s_add_i32 s24, s1, 0xfffffbc0
	s_mul_i32 s25, s24, 0xfc1
	s_lshr_b32 s25, s25, 23
	s_mulk_i32 s25, 0x820
	s_sub_i32 s25, s24, s25
	s_bfe_u32 s33, s25, 0xb0005
	s_cmpk_gt_u32 s24, 0x81f
	s_mov_b64 s[82:83], -1
	s_cbranch_scc0 .LBB0_510
	s_add_i32 s24, s1, 0xfffff3a0
	s_and_b32 s50, 0xffff, s25
	s_cmpk_lt_u32 s50, 0x800
	s_cselect_b64 s[80:81], -1, 0
	s_lshl_b32 s72, s33, 20
	s_cmpk_gt_u32 s24, 0x81f
	s_cbranch_scc0 .LBB0_508
	s_lshl_b64 s[50:51], s[72:73], 2
	s_waitcnt lgkmcnt(0)
	s_add_u32 s24, s12, s50
	s_addc_u32 s58, s13, s51
	s_and_b64 s[50:51], s[80:81], exec
	s_cselect_b32 s79, s58, s23
	s_cselect_b32 s78, s24, s22
	s_mov_b64 s[82:83], 0

; #define GAS __attribute__((address_space(1)))
; __device__ __forceinline__ int conv_dst_row(int mode, int n) {
;     if (mode == 1) { if (n >= C_AQ && n < C_AV) { const int hb = n & ~127, dd = n & 127; return hb + (dd < 64 ? 2 * dd : 2 * (dd - 64) + 1); } return n; }
;     if (mode == 2) return (n >> 7) * 256 + (n & 127);
;     if (mode == 3) return (n >> 7) * 256 + 128 + (n & 127);
;     return n;
; }
; __device__ __forceinline__ void conv8_store(const ConvJob& J, int tid, const f32x4 (&v)[16]) {
;     const int nblk = J.ncols / 256, k0 = 128 * (J.item / nblk), n0 = J.ncol0 + 256 * (J.item % nblk);
;     const int lane = tid & 63, w = tid >> 6, kg = lane & 7, nq = lane >> 3; const float sc8 = J.sc8;
; #pragma unroll
;     for (int c = 0; c < 4; ++c) { u32x4 o;
; #pragma unroll
;         for (int d = 0; d < 4; ++d) { int wv = __builtin_amdgcn_cvt_pk_fp8_f32(v[4 * d][c] * sc8, v[4 * d + 1][c] * sc8, 0, false);
;             wv = __builtin_amdgcn_cvt_pk_fp8_f32(v[4 * d + 2][c] * sc8, v[4 * d + 3][c] * sc8, wv, true); o[d] = (unsigned)wv; }
;         *(GAS u32x4*)(J.WT + (size_t)conv_dst_row(J.mode, n0 - J.ncol0 + 32 * w + 4 * nq + c) * J.K + k0 + 16 * kg) = o; }
.LBB0_564:
	v_mul_f32_e32 v141, s24, v46
	v_mul_f32_e32 v143, s24, v50
	v_mov_b32_e32 v142, v163
	v_cvt_pk_fp8_f32 v142, v141, v143
	v_mul_f32_e32 v145, s24, v74
	v_mul_f32_e32 v146, s24, v82
	v_mov_b32_e32 v143, v163
	v_cvt_pk_fp8_f32 v143, v145, v146
	v_mul_f32_e32 v141, s24, v58
	v_mul_f32_e32 v144, s24, v66
	v_cvt_pk_fp8_f32 v142, v141, v144 op_sel:[0,0,1]
	v_mul_f32_e32 v141, s24, v86
	v_mul_f32_e32 v144, s24, v94
	v_cvt_pk_fp8_f32 v143, v141, v144 op_sel:[0,0,1]
	v_mul_f32_e32 v141, s24, v98
	v_mul_f32_e32 v145, s24, v102
	v_mov_b32_e32 v144, v163
	v_cvt_pk_fp8_f32 v144, v141, v145
	v_mul_f32_e32 v147, s24, v114
	v_mul_f32_e32 v148, s24, v118
	v_mov_b32_e32 v145, v163
	v_cvt_pk_fp8_f32 v145, v147, v148
	v_mul_f32_e32 v141, s24, v106
	v_mul_f32_e32 v146, s24, v110
	v_cvt_pk_fp8_f32 v144, v141, v146 op_sel:[0,0,1]
	v_mul_f32_e32 v141, s24, v122
	v_mul_f32_e32 v146, s24, v126
	v_cvt_pk_fp8_f32 v145, v141, v146 op_sel:[0,0,1]
	v_ashrrev_i32_e32 v141, 31, v140
	v_mov_b64_e32 v[146:147], s[80:81]
	s_lshl_b32 s82, s51, 7
	v_mad_u64_u32 v[146:147], s[50:51], s78, v140, v[146:147]
	v_mul_lo_u32 v140, s79, v140
	v_mul_lo_u32 v141, s78, v141
	s_ashr_i32 s83, s82, 31
	v_add3_u32 v147, v140, v147, v141
	s_add_i32 s33, s33, s25
	v_lshl_add_u64 v[140:141], v[146:147], 0, s[82:83]
	v_add_u32_e32 v139, s33, v135
	v_lshl_add_u64 v[140:141], v[140:141], 0, v[130:131]
	global_store_dwordx4 v[140:141], v[142:145], off nt
	s_cmp_lt_i32 s1, 2
	s_mov_b64 s[84:85], -1
	v_or_b32_e32 v142, 1, v139
	v_subrev_u32_e32 v141, s25, v142
	s_cbranch_scc1 .LBB0_570
	s_cmp_gt_i32 s1, 2
	v_lshlrev_b32_e32 v143, 1, v141
	s_cbranch_scc0 .LBB0_567
	v_and_b32_e32 v140, 0xffffff00, v143
	v_and_b32_e32 v144, 0x7d, v142
	v_or3_b32 v140, v144, v140, s2
	s_mov_b64 s[84:85], 0

; #define GAS __attribute__((address_space(1)))
; __device__ __forceinline__ int conv_dst_row(int mode, int n) {
;     if (mode == 1) { if (n >= C_AQ && n < C_AV) { const int hb = n & ~127, dd = n & 127; return hb + (dd < 64 ? 2 * dd : 2 * (dd - 64) + 1); } return n; }
;     if (mode == 2) return (n >> 7) * 256 + (n & 127);
;     if (mode == 3) return (n >> 7) * 256 + 128 + (n & 127);
;     return n;
; }
; __device__ __forceinline__ void conv8_store(const ConvJob& J, int tid, const f32x4 (&v)[16]) {
;     const int nblk = J.ncols / 256, k0 = 128 * (J.item / nblk), n0 = J.ncol0 + 256 * (J.item % nblk);
;     const int lane = tid & 63, w = tid >> 6, kg = lane & 7, nq = lane >> 3; const float sc8 = J.sc8;
; #pragma unroll
;     for (int c = 0; c < 4; ++c) { u32x4 o;
; #pragma unroll
;         for (int d = 0; d < 4; ++d) { int wv = __builtin_amdgcn_cvt_pk_fp8_f32(v[4 * d][c] * sc8, v[4 * d + 1][c] * sc8, 0, false);
;             wv = __builtin_amdgcn_cvt_pk_fp8_f32(v[4 * d + 2][c] * sc8, v[4 * d + 3][c] * sc8, wv, true); o[d] = (unsigned)wv; }
;         *(GAS u32x4*)(J.WT + (size_t)conv_dst_row(J.mode, n0 - J.ncol0 + 32 * w + 4 * nq + c) * J.K + k0 + 16 * kg) = o; }
.LBB0_574:
	v_mul_f32_e32 v141, s24, v47
	v_mul_f32_e32 v143, s24, v51
	v_mov_b32_e32 v142, v163
	v_cvt_pk_fp8_f32 v142, v141, v143
	v_mul_f32_e32 v145, s24, v75
	v_mul_f32_e32 v146, s24, v83
	v_mov_b32_e32 v143, v163
	v_cvt_pk_fp8_f32 v143, v145, v146
	v_mul_f32_e32 v141, s24, v59
	v_mul_f32_e32 v144, s24, v67
	v_cvt_pk_fp8_f32 v142, v141, v144 op_sel:[0,0,1]
	v_mul_f32_e32 v141, s24, v87
	v_mul_f32_e32 v144, s24, v95
	v_cvt_pk_fp8_f32 v143, v141, v144 op_sel:[0,0,1]
	v_mul_f32_e32 v141, s24, v99
	v_mul_f32_e32 v145, s24, v103
	v_mov_b32_e32 v144, v163
	v_cvt_pk_fp8_f32 v144, v141, v145
	v_mul_f32_e32 v147, s24, v115
	v_mul_f32_e32 v148, s24, v119
	v_mov_b32_e32 v145, v163
	v_cvt_pk_fp8_f32 v145, v147, v148
	v_mul_f32_e32 v141, s24, v107
	v_mul_f32_e32 v146, s24, v111
	v_cvt_pk_fp8_f32 v144, v141, v146 op_sel:[0,0,1]
	v_mul_f32_e32 v141, s24, v123
	v_mul_f32_e32 v146, s24, v127
	v_cvt_pk_fp8_f32 v145, v141, v146 op_sel:[0,0,1]
	v_ashrrev_i32_e32 v141, 31, v140
	v_mov_b64_e32 v[146:147], s[80:81]
	v_mad_u64_u32 v[146:147], s[50:51], s78, v140, v[146:147]
	v_mul_lo_u32 v140, s79, v140
	v_mul_lo_u32 v141, s78, v141
	v_add3_u32 v147, v140, v147, v141
	v_lshl_add_u64 v[140:141], v[146:147], 0, s[82:83]
	v_lshl_add_u64 v[140:141], v[140:141], 0, v[130:131]
	global_store_dwordx4 v[140:141], v[142:145], off nt
	s_cmp_lt_i32 s1, 2
	s_mov_b64 s[84:85], -1
	v_or_b32_e32 v142, 2, v139
	v_subrev_u32_e32 v141, s25, v142
	s_cbranch_scc1 .LBB0_580
	s_cmp_gt_i32 s1, 2
	v_lshlrev_b32_e32 v143, 1, v141
	s_cbranch_scc0 .LBB0_577
	v_and_b32_e32 v140, 0xffffff00, v143
	v_and_b32_e32 v144, 0x7e, v142
	v_or3_b32 v140, v144, v140, s2
	s_mov_b64 s[84:85], 0

; #define GAS __attribute__((address_space(1)))
; __device__ __forceinline__ int conv_dst_row(int mode, int n) {
;     if (mode == 1) { if (n >= C_AQ && n < C_AV) { const int hb = n & ~127, dd = n & 127; return hb + (dd < 64 ? 2 * dd : 2 * (dd - 64) + 1); } return n; }
;     if (mode == 2) return (n >> 7) * 256 + (n & 127);
;     if (mode == 3) return (n >> 7) * 256 + 128 + (n & 127);
;     return n;
; }
; __device__ __forceinline__ void conv8_store(const ConvJob& J, int tid, const f32x4 (&v)[16]) {
;     const int nblk = J.ncols / 256, k0 = 128 * (J.item / nblk), n0 = J.ncol0 + 256 * (J.item % nblk);
;     const int lane = tid & 63, w = tid >> 6, kg = lane & 7, nq = lane >> 3; const float sc8 = J.sc8;
; #pragma unroll
;     for (int c = 0; c < 4; ++c) { u32x4 o;
; #pragma unroll
;         for (int d = 0; d < 4; ++d) { int wv = __builtin_amdgcn_cvt_pk_fp8_f32(v[4 * d][c] * sc8, v[4 * d + 1][c] * sc8, 0, false);
;             wv = __builtin_amdgcn_cvt_pk_fp8_f32(v[4 * d + 2][c] * sc8, v[4 * d + 3][c] * sc8, wv, true); o[d] = (unsigned)wv; }
;         *(GAS u32x4*)(J.WT + (size_t)conv_dst_row(J.mode, n0 - J.ncol0 + 32 * w + 4 * nq + c) * J.K + k0 + 16 * kg) = o; }
.LBB0_584:
	v_mul_f32_e32 v141, s24, v48
	v_mul_f32_e32 v143, s24, v52
	v_mov_b32_e32 v142, v163
	v_cvt_pk_fp8_f32 v142, v141, v143
	v_mul_f32_e32 v145, s24, v76
	v_mul_f32_e32 v146, s24, v84
	v_mov_b32_e32 v143, v163
	v_cvt_pk_fp8_f32 v143, v145, v146
	v_mul_f32_e32 v141, s24, v60
	v_mul_f32_e32 v144, s24, v68
	v_cvt_pk_fp8_f32 v142, v141, v144 op_sel:[0,0,1]
	v_mul_f32_e32 v141, s24, v88
	v_mul_f32_e32 v144, s24, v96
	v_cvt_pk_fp8_f32 v143, v141, v144 op_sel:[0,0,1]
	v_mul_f32_e32 v141, s24, v100
	v_mul_f32_e32 v145, s24, v104
	v_mov_b32_e32 v144, v163
	v_cvt_pk_fp8_f32 v144, v141, v145
	v_mul_f32_e32 v147, s24, v116
	v_mul_f32_e32 v148, s24, v120
	v_mov_b32_e32 v145, v163
	v_cvt_pk_fp8_f32 v145, v147, v148
	v_mul_f32_e32 v141, s24, v108
	v_mul_f32_e32 v146, s24, v112
	v_cvt_pk_fp8_f32 v144, v141, v146 op_sel:[0,0,1]
	v_mul_f32_e32 v141, s24, v124
	v_mul_f32_e32 v146, s24, v128
	v_cvt_pk_fp8_f32 v145, v141, v146 op_sel:[0,0,1]
	v_ashrrev_i32_e32 v141, 31, v140
	v_mov_b64_e32 v[146:147], s[80:81]
	v_mad_u64_u32 v[146:147], s[50:51], s78, v140, v[146:147]
	v_mul_lo_u32 v140, s79, v140
	v_mul_lo_u32 v141, s78, v141
	v_add3_u32 v147, v140, v147, v141
	v_lshl_add_u64 v[140:141], v[146:147], 0, s[82:83]
	v_lshl_add_u64 v[140:141], v[140:141], 0, v[130:131]
	global_store_dwordx4 v[140:141], v[142:145], off nt
	v_or_b32_e32 v141, 3, v139
	v_subrev_u32_e32 v140, s25, v141
	s_cmp_lt_i32 s1, 2
	s_mov_b64 s[84:85], -1
	s_cbranch_scc1 .LBB0_590
	s_cmp_gt_i32 s1, 2
	v_lshlrev_b32_e32 v142, 1, v140
	s_cbranch_scc0 .LBB0_587
	v_and_b32_e32 v139, 0xffffff00, v142
	v_and_b32_e32 v143, 0x7f, v141
	v_or3_b32 v139, v143, v139, s2
	s_mov_b64 s[84:85], 0

; #define GAS __attribute__((address_space(1)))
; __device__ __forceinline__ void conv8_store(const ConvJob& J, int tid, const f32x4 (&v)[16]) {
;     const int nblk = J.ncols / 256, k0 = 128 * (J.item / nblk), n0 = J.ncol0 + 256 * (J.item % nblk);
;     const int lane = tid & 63, w = tid >> 6, kg = lane & 7, nq = lane >> 3; const float sc8 = J.sc8;
; #pragma unroll
;     for (int c = 0; c < 4; ++c) { u32x4 o;
; #pragma unroll
;         for (int d = 0; d < 4; ++d) { int wv = __builtin_amdgcn_cvt_pk_fp8_f32(v[4 * d][c] * sc8, v[4 * d + 1][c] * sc8, 0, false);
;             wv = __builtin_amdgcn_cvt_pk_fp8_f32(v[4 * d + 2][c] * sc8, v[4 * d + 3][c] * sc8, wv, true); o[d] = (unsigned)wv; }
;         *(GAS u32x4*)(J.WT + (size_t)conv_dst_row(J.mode, n0 - J.ncol0 + 32 * w + 4 * nq + c) * J.K + k0 + 16 * kg) = o; }
.LBB0_598:
	v_mul_f32_e32 v7, s26, v29
	v_mul_f32_e32 v8, s26, v33
	v_mov_b32_e32 v6, v71
	v_cvt_pk_fp8_f32 v6, v7, v8
	v_mul_f32_e32 v8, s26, v45
	v_mul_f32_e32 v10, s26, v49
	v_mov_b32_e32 v7, v71
	v_cvt_pk_fp8_f32 v7, v8, v10
	v_mul_f32_e32 v9, s26, v9
	v_mul_f32_e32 v10, s26, v21
	v_mov_b32_e32 v8, v71
	v_cvt_pk_fp8_f32 v8, v9, v10
	v_mul_f32_e32 v10, s26, v13
	v_mul_f32_e32 v11, s26, v25
	v_mov_b32_e32 v9, v71
	v_mul_f32_e32 v3, s26, v61
	v_mul_f32_e32 v4, s26, v65
	v_cvt_pk_fp8_f32 v9, v10, v11
	v_cvt_pk_fp8_f32 v6, v3, v4 op_sel:[0,0,1]
	v_mul_f32_e32 v3, s26, v37
	v_mul_f32_e32 v4, s26, v41
	v_cvt_pk_fp8_f32 v7, v3, v4 op_sel:[0,0,1]
	v_mul_f32_e32 v3, s26, v53
	v_mul_f32_e32 v4, s26, v57
	v_cvt_pk_fp8_f32 v8, v3, v4 op_sel:[0,0,1]
	v_mul_f32_e32 v3, s26, v5
	v_mul_f32_e32 v4, s26, v17
	v_cvt_pk_fp8_f32 v9, v3, v4 op_sel:[0,0,1]
	v_ashrrev_i32_e32 v3, 31, v2
	v_mov_b64_e32 v[4:5], s[48:49]
	v_mad_u64_u32 v[4:5], s[26:27], s36, v2, v[4:5]
	v_mul_lo_u32 v2, s37, v2
	v_mul_lo_u32 v3, s36, v3
	v_add3_u32 v5, v2, v5, v3
	v_lshl_add_u64 v[2:3], v[4:5], 0, s[58:59]
	v_lshl_add_u64 v[2:3], v[2:3], 0, v[66:67]
	s_mov_b64 s[36:37], 0
	global_store_dwordx4 v[2:3], v[6:9], off nt

; #define GAS __attribute__((address_space(1)))
; __device__ __forceinline__ int conv_dst_row(int mode, int n) {
;     if (mode == 1) { if (n >= C_AQ && n < C_AV) { const int hb = n & ~127, dd = n & 127; return hb + (dd < 64 ? 2 * dd : 2 * (dd - 64) + 1); } return n; }
;     if (mode == 2) return (n >> 7) * 256 + (n & 127);
;     if (mode == 3) return (n >> 7) * 256 + 128 + (n & 127);
;     return n;
; __device__ __forceinline__ void conv8_store(const ConvJob& J, int tid, const f32x4 (&v)[16]) {
;     const int nblk = J.ncols / 256, k0 = 128 * (J.item / nblk), n0 = J.ncol0 + 256 * (J.item % nblk);
;     const int lane = tid & 63, w = tid >> 6, kg = lane & 7, nq = lane >> 3; const float sc8 = J.sc8;
; #pragma unroll
;     for (int c = 0; c < 4; ++c) { u32x4 o;
; #pragma unroll
;         for (int d = 0; d < 4; ++d) { int wv = __builtin_amdgcn_cvt_pk_fp8_f32(v[4 * d][c] * sc8, v[4 * d + 1][c] * sc8, 0, false);
;             wv = __builtin_amdgcn_cvt_pk_fp8_f32(v[4 * d + 2][c] * sc8, v[4 * d + 3][c] * sc8, wv, true); o[d] = (unsigned)wv; }
;         *(GAS u32x4*)(J.WT + (size_t)conv_dst_row(J.mode, n0 - J.ncol0 + 32 * w + 4 * nq + c) * J.K + k0 + 16 * kg) = o; }
.LBB0_641:
	s_waitcnt vmcnt(7)
	v_mul_f32_e32 v6, s26, v6
	s_waitcnt vmcnt(6)
	v_mul_f32_e32 v18, s26, v18
	v_mov_b32_e32 v80, v71
	v_mul_f32_e32 v26, s26, v26
	v_mul_f32_e32 v30, s26, v30
	v_mov_b32_e32 v78, v71
	v_cvt_pk_fp8_f32 v80, v6, v18
	s_waitcnt vmcnt(3)
	v_mul_f32_e32 v10, s26, v10
	s_waitcnt vmcnt(2)
	v_mul_f32_e32 v22, s26, v22
	v_mov_b32_e32 v81, v71
	v_cvt_pk_fp8_f32 v78, v26, v30
	v_mul_f32_e32 v42, s26, v42
	v_mul_f32_e32 v46, s26, v46
	v_mov_b32_e32 v79, v71
	v_cvt_pk_fp8_f32 v81, v10, v22
	v_cvt_pk_fp8_f32 v79, v42, v46
	v_mul_f32_e32 v6, s26, v50
	v_mul_f32_e32 v18, s26, v54
	v_mul_f32_e32 v26, s26, v58
	v_mul_f32_e32 v30, s26, v62
	v_cvt_pk_fp8_f32 v80, v6, v18 op_sel:[0,0,1]
	s_waitcnt vmcnt(1)
	v_mul_f32_e32 v2, s26, v2
	s_waitcnt vmcnt(0)
	v_mul_f32_e32 v6, s26, v14
	v_cvt_pk_fp8_f32 v78, v26, v30 op_sel:[0,0,1]
	v_mul_f32_e32 v26, s26, v34
	v_mul_f32_e32 v30, s26, v38
	v_cvt_pk_fp8_f32 v81, v2, v6 op_sel:[0,0,1]
	v_ashrrev_i32_e32 v2, 31, v77
	v_mov_b64_e32 v[82:83], s[48:49]
	v_cvt_pk_fp8_f32 v79, v26, v30 op_sel:[0,0,1]
	v_mad_u64_u32 v[82:83], s[50:51], s36, v77, v[82:83]
	v_mul_lo_u32 v6, s37, v77
	v_mul_lo_u32 v2, s36, v2
	v_add_u32_e32 v76, s64, v1
	v_add3_u32 v83, v6, v83, v2
	v_lshl_add_u64 v[82:83], v[82:83], 0, s[58:59]
	v_or_b32_e32 v10, 1, v76
	v_lshl_add_u64 v[82:83], v[82:83], 0, v[66:67]
	v_subrev_u32_e32 v6, s27, v10
	s_cmp_lt_i32 s25, 2
	s_mov_b64 s[60:61], -1
	global_store_dwordx4 v[82:83], v[78:81], off nt
	s_cbranch_scc1 .LBB0_647
	s_cmp_gt_i32 s25, 2
	v_lshlrev_b32_e32 v14, 1, v6
	s_cbranch_scc0 .LBB0_644
	v_and_b32_e32 v2, 0xffffff00, v14
	v_and_b32_e32 v18, 0x7d, v10
	v_or3_b32 v2, v18, v2, s1
	s_mov_b64 s[60:61], 0

; #define GAS __attribute__((address_space(1)))
; __device__ __forceinline__ int conv_dst_row(int mode, int n) {
;     if (mode == 1) { if (n >= C_AQ && n < C_AV) { const int hb = n & ~127, dd = n & 127; return hb + (dd < 64 ? 2 * dd : 2 * (dd - 64) + 1); } return n; }
;     if (mode == 2) return (n >> 7) * 256 + (n & 127);
;     if (mode == 3) return (n >> 7) * 256 + 128 + (n & 127);
;     return n;
; __device__ __forceinline__ void conv8_store(const ConvJob& J, int tid, const f32x4 (&v)[16]) {
;     const int nblk = J.ncols / 256, k0 = 128 * (J.item / nblk), n0 = J.ncol0 + 256 * (J.item % nblk);
;     const int lane = tid & 63, w = tid >> 6, kg = lane & 7, nq = lane >> 3; const float sc8 = J.sc8;
; #pragma unroll
;     for (int c = 0; c < 4; ++c) { u32x4 o;
; #pragma unroll
;         for (int d = 0; d < 4; ++d) { int wv = __builtin_amdgcn_cvt_pk_fp8_f32(v[4 * d][c] * sc8, v[4 * d + 1][c] * sc8, 0, false);
;             wv = __builtin_amdgcn_cvt_pk_fp8_f32(v[4 * d + 2][c] * sc8, v[4 * d + 3][c] * sc8, wv, true); o[d] = (unsigned)wv; }
;         *(GAS u32x4*)(J.WT + (size_t)conv_dst_row(J.mode, n0 - J.ncol0 + 32 * w + 4 * nq + c) * J.K + k0 + 16 * kg) = o; }
.LBB0_651:
	v_mul_f32_e32 v6, s26, v27
	v_mul_f32_e32 v10, s26, v31
	v_mov_b32_e32 v78, v71
	v_cvt_pk_fp8_f32 v78, v6, v10
	v_mul_f32_e32 v14, s26, v43
	v_mul_f32_e32 v18, s26, v47
	v_mov_b32_e32 v79, v71
	v_cvt_pk_fp8_f32 v79, v14, v18
	v_mul_f32_e32 v6, s26, v59
	v_mul_f32_e32 v10, s26, v63
	v_cvt_pk_fp8_f32 v78, v6, v10 op_sel:[0,0,1]
	v_mul_f32_e32 v6, s26, v35
	v_mul_f32_e32 v10, s26, v39
	v_cvt_pk_fp8_f32 v79, v6, v10 op_sel:[0,0,1]
	v_mul_f32_e32 v6, s26, v7
	v_mul_f32_e32 v7, s26, v19
	v_mov_b32_e32 v80, v71
	v_cvt_pk_fp8_f32 v80, v6, v7
	v_mul_f32_e32 v10, s26, v11
	v_mul_f32_e32 v11, s26, v23
	v_mov_b32_e32 v81, v71
	v_cvt_pk_fp8_f32 v81, v10, v11
	v_mul_f32_e32 v6, s26, v51
	v_mul_f32_e32 v7, s26, v55
	v_cvt_pk_fp8_f32 v80, v6, v7 op_sel:[0,0,1]
	v_mul_f32_e32 v3, s26, v3
	v_mul_f32_e32 v6, s26, v15
	v_cvt_pk_fp8_f32 v81, v3, v6 op_sel:[0,0,1]
	v_ashrrev_i32_e32 v3, 31, v2
	v_mov_b64_e32 v[6:7], s[48:49]
	v_mad_u64_u32 v[6:7], s[50:51], s36, v2, v[6:7]
	v_mul_lo_u32 v2, s37, v2
	v_mul_lo_u32 v3, s36, v3
	v_add3_u32 v7, v2, v7, v3
	v_lshl_add_u64 v[2:3], v[6:7], 0, s[58:59]
	v_lshl_add_u64 v[2:3], v[2:3], 0, v[66:67]
	v_or_b32_e32 v6, 2, v76
	global_store_dwordx4 v[2:3], v[78:81], off nt
	v_subrev_u32_e32 v3, s27, v6
	s_cmp_lt_i32 s25, 2
	s_mov_b64 s[60:61], -1
	s_cbranch_scc1 .LBB0_657
	s_cmp_gt_i32 s25, 2
	v_lshlrev_b32_e32 v7, 1, v3
	s_cbranch_scc0 .LBB0_654
	v_and_b32_e32 v2, 0xffffff00, v7
	v_and_b32_e32 v10, 0x7e, v6
	v_or3_b32 v2, v10, v2, s1
	s_mov_b64 s[60:61], 0

; #define GAS __attribute__((address_space(1)))
; __device__ __forceinline__ int conv_dst_row(int mode, int n) {
;     if (mode == 1) { if (n >= C_AQ && n < C_AV) { const int hb = n & ~127, dd = n & 127; return hb + (dd < 64 ? 2 * dd : 2 * (dd - 64) + 1); } return n; }
;     if (mode == 2) return (n >> 7) * 256 + (n & 127);
;     if (mode == 3) return (n >> 7) * 256 + 128 + (n & 127);
;     return n;
; __device__ __forceinline__ void conv8_store(const ConvJob& J, int tid, const f32x4 (&v)[16]) {
;     const int nblk = J.ncols / 256, k0 = 128 * (J.item / nblk), n0 = J.ncol0 + 256 * (J.item % nblk);
;     const int lane = tid & 63, w = tid >> 6, kg = lane & 7, nq = lane >> 3; const float sc8 = J.sc8;
; #pragma unroll
;     for (int c = 0; c < 4; ++c) { u32x4 o;
; #pragma unroll
;         for (int d = 0; d < 4; ++d) { int wv = __builtin_amdgcn_cvt_pk_fp8_f32(v[4 * d][c] * sc8, v[4 * d + 1][c] * sc8, 0, false);
;             wv = __builtin_amdgcn_cvt_pk_fp8_f32(v[4 * d + 2][c] * sc8, v[4 * d + 3][c] * sc8, wv, true); o[d] = (unsigned)wv; }
;         *(GAS u32x4*)(J.WT + (size_t)conv_dst_row(J.mode, n0 - J.ncol0 + 32 * w + 4 * nq + c) * J.K + k0 + 16 * kg) = o; }
.LBB0_661:
	v_mul_f32_e32 v3, s26, v28
	v_mul_f32_e32 v6, s26, v32
	v_mov_b32_e32 v78, v71
	v_cvt_pk_fp8_f32 v78, v3, v6
	v_mul_f32_e32 v7, s26, v44
	v_mul_f32_e32 v10, s26, v48
	v_mov_b32_e32 v79, v71
	v_cvt_pk_fp8_f32 v79, v7, v10
	v_mul_f32_e32 v3, s26, v60
	v_mul_f32_e32 v6, s26, v64
	v_cvt_pk_fp8_f32 v78, v3, v6 op_sel:[0,0,1]
	v_mul_f32_e32 v3, s26, v36
	v_mul_f32_e32 v6, s26, v40
	v_cvt_pk_fp8_f32 v79, v3, v6 op_sel:[0,0,1]
	v_mul_f32_e32 v3, s26, v8
	v_mul_f32_e32 v6, s26, v20
	v_mov_b32_e32 v80, v71
	v_cvt_pk_fp8_f32 v80, v3, v6
	v_mul_f32_e32 v7, s26, v12
	v_mul_f32_e32 v8, s26, v24
	v_mov_b32_e32 v81, v71
	v_cvt_pk_fp8_f32 v81, v7, v8
	v_mul_f32_e32 v3, s26, v52
	v_mul_f32_e32 v6, s26, v56
	v_cvt_pk_fp8_f32 v80, v3, v6 op_sel:[0,0,1]
	v_mul_f32_e32 v3, s26, v4
	v_mul_f32_e32 v4, s26, v16
	v_cvt_pk_fp8_f32 v81, v3, v4 op_sel:[0,0,1]
	v_ashrrev_i32_e32 v3, 31, v2
	v_mov_b64_e32 v[6:7], s[48:49]
	v_mad_u64_u32 v[6:7], s[50:51], s36, v2, v[6:7]
	v_mul_lo_u32 v2, s37, v2
	v_mul_lo_u32 v3, s36, v3
	v_add3_u32 v7, v2, v7, v3
	v_lshl_add_u64 v[2:3], v[6:7], 0, s[58:59]
	v_lshl_add_u64 v[2:3], v[2:3], 0, v[66:67]
	v_or_b32_e32 v4, 3, v76
	global_store_dwordx4 v[2:3], v[78:81], off nt
	v_subrev_u32_e32 v3, s27, v4
	s_cmp_lt_i32 s25, 2
	s_mov_b64 s[60:61], -1
	s_cbranch_scc1 .LBB0_667
	s_cmp_gt_i32 s25, 2
	v_lshlrev_b32_e32 v6, 1, v3
	s_cbranch_scc0 .LBB0_664
	v_and_b32_e32 v2, 0xffffff00, v6
	v_and_b32_e32 v7, 0x7f, v4
	v_or3_b32 v2, v7, v2, s1
	s_mov_b64 s[60:61], 0

; #define GAS __attribute__((address_space(1)))
; __device__ __forceinline__ void conv8_store(const ConvJob& J, int tid, const f32x4 (&v)[16]) {
;     const int nblk = J.ncols / 256, k0 = 128 * (J.item / nblk), n0 = J.ncol0 + 256 * (J.item % nblk);
;     const int lane = tid & 63, w = tid >> 6, kg = lane & 7, nq = lane >> 3; const float sc8 = J.sc8;
; #pragma unroll
;     for (int c = 0; c < 4; ++c) { u32x4 o;
; #pragma unroll
;         for (int d = 0; d < 4; ++d) { int wv = __builtin_amdgcn_cvt_pk_fp8_f32(v[4 * d][c] * sc8, v[4 * d + 1][c] * sc8, 0, false);
;             wv = __builtin_amdgcn_cvt_pk_fp8_f32(v[4 * d + 2][c] * sc8, v[4 * d + 3][c] * sc8, wv, true); o[d] = (unsigned)wv; }
;         *(GAS u32x4*)(J.WT + (size_t)conv_dst_row(J.mode, n0 - J.ncol0 + 32 * w + 4 * nq + c) * J.K + k0 + 16 * kg) = o; }
;     ...
;                 const int q1 = q + F.G; const bool m1 = q1 < q_hi;
;                 if (m1) conv8_load(decode(q1 < I_IN ? q1 : q1 + NB16), tid, vb);
.LBB0_1590:
	v_mul_f32_e32 v143, s38, v49
	v_mul_f32_e32 v145, s38, v53
	v_mov_b32_e32 v142, v163
	v_cvt_pk_fp8_f32 v142, v143, v145
	v_mul_f32_e32 v145, s38, v77
	v_mul_f32_e32 v146, s38, v85
	v_mov_b32_e32 v143, v163
	v_cvt_pk_fp8_f32 v143, v145, v146
	v_mul_f32_e32 v141, s38, v61
	v_mul_f32_e32 v144, s38, v69
	v_cvt_pk_fp8_f32 v142, v141, v144 op_sel:[0,0,1]
	v_mul_f32_e32 v141, s38, v89
	v_mul_f32_e32 v144, s38, v97
	v_cvt_pk_fp8_f32 v143, v141, v144 op_sel:[0,0,1]
	v_mul_f32_e32 v145, s38, v101
	v_mul_f32_e32 v147, s38, v105
	v_mov_b32_e32 v144, v163
	v_cvt_pk_fp8_f32 v144, v145, v147
	v_mul_f32_e32 v147, s38, v117
	v_mul_f32_e32 v148, s38, v121
	v_mov_b32_e32 v145, v163
	v_cvt_pk_fp8_f32 v145, v147, v148
	v_mul_f32_e32 v141, s38, v109
	v_mul_f32_e32 v146, s38, v113
	v_cvt_pk_fp8_f32 v144, v141, v146 op_sel:[0,0,1]
	v_mul_f32_e32 v141, s38, v125
	v_mul_f32_e32 v146, s38, v129
	v_cvt_pk_fp8_f32 v145, v141, v146 op_sel:[0,0,1]
	v_ashrrev_i32_e32 v141, 31, v140
	v_mov_b64_e32 v[146:147], s[76:77]
	v_mad_u64_u32 v[146:147], s[38:39], s74, v140, v[146:147]
	v_mul_lo_u32 v140, s75, v140
	v_mul_lo_u32 v141, s74, v141
	s_add_i32 s13, s12, s1
	v_add3_u32 v147, v140, v147, v141
	v_lshl_add_u64 v[140:141], v[146:147], 0, s[78:79]
	s_cmpk_gt_i32 s13, 0x13ff
	v_lshl_add_u64 v[140:141], v[140:141], 0, v[130:131]
	s_cselect_b64 s[74:75], -1, 0
	global_store_dwordx4 v[140:141], v[142:145], off nt

; #define GAS __attribute__((address_space(1)))
; __device__ __forceinline__ int conv_dst_row(int mode, int n) {
;     if (mode == 1) { if (n >= C_AQ && n < C_AV) { const int hb = n & ~127, dd = n & 127; return hb + (dd < 64 ? 2 * dd : 2 * (dd - 64) + 1); } return n; }
;     if (mode == 2) return (n >> 7) * 256 + (n & 127);
;     if (mode == 3) return (n >> 7) * 256 + 128 + (n & 127);
;     return n;
; __device__ __forceinline__ void conv8_store(const ConvJob& J, int tid, const f32x4 (&v)[16]) {
;     const int nblk = J.ncols / 256, k0 = 128 * (J.item / nblk), n0 = J.ncol0 + 256 * (J.item % nblk);
;     const int lane = tid & 63, w = tid >> 6, kg = lane & 7, nq = lane >> 3; const float sc8 = J.sc8;
; #pragma unroll
;     for (int c = 0; c < 4; ++c) { u32x4 o;
; #pragma unroll
;         for (int d = 0; d < 4; ++d) { int wv = __builtin_amdgcn_cvt_pk_fp8_f32(v[4 * d][c] * sc8, v[4 * d + 1][c] * sc8, 0, false);
;             wv = __builtin_amdgcn_cvt_pk_fp8_f32(v[4 * d + 2][c] * sc8, v[4 * d + 3][c] * sc8, wv, true); o[d] = (unsigned)wv; }
;         *(GAS u32x4*)(J.WT + (size_t)conv_dst_row(J.mode, n0 - J.ncol0 + 32 * w + 4 * nq + c) * J.K + k0 + 16 * kg) = o; }
.LBB0_1656:
	s_waitcnt vmcnt(19)
	v_mul_f32_e32 v143, s39, v2
	s_waitcnt vmcnt(18)
	v_mul_f32_e32 v144, s39, v6
	v_mov_b32_e32 v142, v163
	v_cvt_pk_fp8_f32 v142, v143, v144
	s_waitcnt vmcnt(11)
	v_mul_f32_e32 v146, s39, v18
	s_waitcnt vmcnt(10)
	v_mul_f32_e32 v147, s39, v22
	v_mov_b32_e32 v143, v163
	v_cvt_pk_fp8_f32 v143, v146, v147
	v_mul_f32_e32 v144, s39, v10
	v_mul_f32_e32 v145, s39, v14
	v_cvt_pk_fp8_f32 v142, v144, v145 op_sel:[0,0,1]
	s_waitcnt vmcnt(9)
	v_mul_f32_e32 v144, s39, v26
	s_waitcnt vmcnt(8)
	v_mul_f32_e32 v145, s39, v30
	v_cvt_pk_fp8_f32 v143, v144, v145 op_sel:[0,0,1]
	s_waitcnt vmcnt(7)
	v_mul_f32_e32 v145, s39, v34
	s_waitcnt vmcnt(6)
	v_mul_f32_e32 v146, s39, v38
	v_mov_b32_e32 v144, v163
	v_cvt_pk_fp8_f32 v144, v145, v146
	s_waitcnt vmcnt(3)
	v_mul_f32_e32 v148, s39, v62
	s_waitcnt vmcnt(2)
	v_mul_f32_e32 v149, s39, v70
	v_mov_b32_e32 v145, v163
	v_cvt_pk_fp8_f32 v145, v148, v149
	v_mul_f32_e32 v146, s39, v42
	v_mul_f32_e32 v147, s39, v54
	v_cvt_pk_fp8_f32 v144, v146, v147 op_sel:[0,0,1]
	s_waitcnt vmcnt(1)
	v_mul_f32_e32 v146, s39, v78
	s_waitcnt vmcnt(0)
	v_mul_f32_e32 v147, s39, v90
	v_cvt_pk_fp8_f32 v145, v146, v147 op_sel:[0,0,1]
	v_ashrrev_i32_e32 v148, 31, v141
	v_mov_b64_e32 v[146:147], s[78:79]
	s_lshl_b32 s80, s49, 7
	v_mad_u64_u32 v[146:147], s[60:61], s76, v141, v[146:147]
	v_mul_lo_u32 v141, s77, v141
	v_mul_lo_u32 v148, s76, v148
	s_ashr_i32 s81, s80, 31
	v_add3_u32 v147, v141, v147, v148
	s_add_i32 s45, s45, s44
	v_lshl_add_u64 v[146:147], v[146:147], 0, s[80:81]
	v_add_u32_e32 v140, s45, v136
	v_lshl_add_u64 v[146:147], v[146:147], 0, v[130:131]
	global_store_dwordx4 v[146:147], v[142:145], off nt
	s_cmp_lt_i32 s38, 2
	s_mov_b64 s[82:83], -1
	v_or_b32_e32 v143, 1, v140
	v_subrev_u32_e32 v142, s44, v143
	s_cbranch_scc1 .LBB0_1662
	s_cmp_gt_i32 s38, 2
	v_lshlrev_b32_e32 v144, 1, v142
	s_cbranch_scc0 .LBB0_1659
	v_and_b32_e32 v141, 0xffffff00, v144
	v_and_b32_e32 v145, 0x7d, v143
	v_or3_b32 v141, v145, v141, s5
	s_mov_b64 s[82:83], 0

; #define GAS __attribute__((address_space(1)))
; __device__ __forceinline__ int conv_dst_row(int mode, int n) {
;     if (mode == 1) { if (n >= C_AQ && n < C_AV) { const int hb = n & ~127, dd = n & 127; return hb + (dd < 64 ? 2 * dd : 2 * (dd - 64) + 1); } return n; }
;     if (mode == 2) return (n >> 7) * 256 + (n & 127);
;     if (mode == 3) return (n >> 7) * 256 + 128 + (n & 127);
;     return n;
; __device__ __forceinline__ void conv8_store(const ConvJob& J, int tid, const f32x4 (&v)[16]) {
;     const int nblk = J.ncols / 256, k0 = 128 * (J.item / nblk), n0 = J.ncol0 + 256 * (J.item % nblk);
;     const int lane = tid & 63, w = tid >> 6, kg = lane & 7, nq = lane >> 3; const float sc8 = J.sc8;
; #pragma unroll
;     for (int c = 0; c < 4; ++c) { u32x4 o;
; #pragma unroll
;         for (int d = 0; d < 4; ++d) { int wv = __builtin_amdgcn_cvt_pk_fp8_f32(v[4 * d][c] * sc8, v[4 * d + 1][c] * sc8, 0, false);
;             wv = __builtin_amdgcn_cvt_pk_fp8_f32(v[4 * d + 2][c] * sc8, v[4 * d + 3][c] * sc8, wv, true); o[d] = (unsigned)wv; }
;         *(GAS u32x4*)(J.WT + (size_t)conv_dst_row(J.mode, n0 - J.ncol0 + 32 * w + 4 * nq + c) * J.K + k0 + 16 * kg) = o; }
.LBB0_1666:
	v_mul_f32_e32 v143, s39, v3
	v_mul_f32_e32 v144, s39, v7
	v_mov_b32_e32 v142, v163
	v_cvt_pk_fp8_f32 v142, v143, v144
	v_mul_f32_e32 v146, s39, v19
	v_mul_f32_e32 v147, s39, v23
	v_mov_b32_e32 v143, v163
	v_cvt_pk_fp8_f32 v143, v146, v147
	v_mul_f32_e32 v144, s39, v11
	v_mul_f32_e32 v145, s39, v15
	v_cvt_pk_fp8_f32 v142, v144, v145 op_sel:[0,0,1]
	v_mul_f32_e32 v144, s39, v27
	v_mul_f32_e32 v145, s39, v31
	v_cvt_pk_fp8_f32 v143, v144, v145 op_sel:[0,0,1]
	v_mul_f32_e32 v145, s39, v35
	v_mul_f32_e32 v146, s39, v39
	v_mov_b32_e32 v144, v163
	v_cvt_pk_fp8_f32 v144, v145, v146
	v_mul_f32_e32 v148, s39, v63
	v_mul_f32_e32 v149, s39, v71
	v_mov_b32_e32 v145, v163
	v_cvt_pk_fp8_f32 v145, v148, v149
	v_mul_f32_e32 v146, s39, v43
	v_mul_f32_e32 v147, s39, v55
	v_cvt_pk_fp8_f32 v144, v146, v147 op_sel:[0,0,1]
	v_mul_f32_e32 v146, s39, v79
	v_mul_f32_e32 v147, s39, v91
	v_cvt_pk_fp8_f32 v145, v146, v147 op_sel:[0,0,1]
	v_ashrrev_i32_e32 v148, 31, v141
	v_mov_b64_e32 v[146:147], s[78:79]
	v_mad_u64_u32 v[146:147], s[60:61], s76, v141, v[146:147]
	v_mul_lo_u32 v141, s77, v141
	v_mul_lo_u32 v148, s76, v148
	v_add3_u32 v147, v141, v147, v148
	v_lshl_add_u64 v[146:147], v[146:147], 0, s[80:81]
	v_lshl_add_u64 v[146:147], v[146:147], 0, v[130:131]
	global_store_dwordx4 v[146:147], v[142:145], off nt
	s_cmp_lt_i32 s38, 2
	s_mov_b64 s[82:83], -1
	v_or_b32_e32 v143, 2, v140
	v_subrev_u32_e32 v142, s44, v143
	s_cbranch_scc1 .LBB0_1672
	s_cmp_gt_i32 s38, 2
	v_lshlrev_b32_e32 v144, 1, v142
	s_cbranch_scc0 .LBB0_1669
	v_and_b32_e32 v141, 0xffffff00, v144
	v_and_b32_e32 v145, 0x7e, v143
	v_or3_b32 v141, v145, v141, s5
	s_mov_b64 s[82:83], 0

; #define GAS __attribute__((address_space(1)))
; __device__ __forceinline__ int conv_dst_row(int mode, int n) {
;     if (mode == 1) { if (n >= C_AQ && n < C_AV) { const int hb = n & ~127, dd = n & 127; return hb + (dd < 64 ? 2 * dd : 2 * (dd - 64) + 1); } return n; }
;     if (mode == 2) return (n >> 7) * 256 + (n & 127);
;     if (mode == 3) return (n >> 7) * 256 + 128 + (n & 127);
;     return n;
; __device__ __forceinline__ void conv8_store(const ConvJob& J, int tid, const f32x4 (&v)[16]) {
;     const int nblk = J.ncols / 256, k0 = 128 * (J.item / nblk), n0 = J.ncol0 + 256 * (J.item % nblk);
;     const int lane = tid & 63, w = tid >> 6, kg = lane & 7, nq = lane >> 3; const float sc8 = J.sc8;
; #pragma unroll
;     for (int c = 0; c < 4; ++c) { u32x4 o;
; #pragma unroll
;         for (int d = 0; d < 4; ++d) { int wv = __builtin_amdgcn_cvt_pk_fp8_f32(v[4 * d][c] * sc8, v[4 * d + 1][c] * sc8, 0, false);
;             wv = __builtin_amdgcn_cvt_pk_fp8_f32(v[4 * d + 2][c] * sc8, v[4 * d + 3][c] * sc8, wv, true); o[d] = (unsigned)wv; }
;         *(GAS u32x4*)(J.WT + (size_t)conv_dst_row(J.mode, n0 - J.ncol0 + 32 * w + 4 * nq + c) * J.K + k0 + 16 * kg) = o; }
.LBB0_1676:
	v_mul_f32_e32 v143, s39, v4
	v_mul_f32_e32 v144, s39, v8
	v_mov_b32_e32 v142, v163
	v_cvt_pk_fp8_f32 v142, v143, v144
	v_mul_f32_e32 v146, s39, v20
	v_mul_f32_e32 v147, s39, v24
	v_mov_b32_e32 v143, v163
	v_cvt_pk_fp8_f32 v143, v146, v147
	v_mul_f32_e32 v144, s39, v12
	v_mul_f32_e32 v145, s39, v16
	v_cvt_pk_fp8_f32 v142, v144, v145 op_sel:[0,0,1]
	v_mul_f32_e32 v144, s39, v28
	v_mul_f32_e32 v145, s39, v32
	v_cvt_pk_fp8_f32 v143, v144, v145 op_sel:[0,0,1]
	v_mul_f32_e32 v145, s39, v36
	v_mul_f32_e32 v146, s39, v40
	v_mov_b32_e32 v144, v163
	v_cvt_pk_fp8_f32 v144, v145, v146
	v_mul_f32_e32 v148, s39, v64
	v_mul_f32_e32 v149, s39, v72
	v_mov_b32_e32 v145, v163
	v_cvt_pk_fp8_f32 v145, v148, v149
	v_mul_f32_e32 v146, s39, v44
	v_mul_f32_e32 v147, s39, v56
	v_cvt_pk_fp8_f32 v144, v146, v147 op_sel:[0,0,1]
	v_mul_f32_e32 v146, s39, v80
	v_mul_f32_e32 v147, s39, v92
	v_cvt_pk_fp8_f32 v145, v146, v147 op_sel:[0,0,1]
	v_ashrrev_i32_e32 v148, 31, v141
	v_mov_b64_e32 v[146:147], s[78:79]
	v_mad_u64_u32 v[146:147], s[60:61], s76, v141, v[146:147]
	v_mul_lo_u32 v141, s77, v141
	v_mul_lo_u32 v148, s76, v148
	v_add3_u32 v147, v141, v147, v148
	v_lshl_add_u64 v[146:147], v[146:147], 0, s[80:81]
	v_lshl_add_u64 v[146:147], v[146:147], 0, v[130:131]
	global_store_dwordx4 v[146:147], v[142:145], off nt
	s_cmp_lt_i32 s38, 2
	s_mov_b64 s[82:83], -1
	v_or_b32_e32 v142, 3, v140
	v_subrev_u32_e32 v141, s44, v142
	s_cbranch_scc1 .LBB0_1682
	s_cmp_gt_i32 s38, 2
	v_lshlrev_b32_e32 v143, 1, v141
	s_cbranch_scc0 .LBB0_1679
	v_and_b32_e32 v140, 0xffffff00, v143
	v_and_b32_e32 v144, 0x7f, v142
	v_or3_b32 v140, v144, v140, s5
	s_mov_b64 s[82:83], 0

; #define GAS __attribute__((address_space(1)))
; __device__ __forceinline__ void conv8_store(const ConvJob& J, int tid, const f32x4 (&v)[16]) {
;     const int nblk = J.ncols / 256, k0 = 128 * (J.item / nblk), n0 = J.ncol0 + 256 * (J.item % nblk);
;     const int lane = tid & 63, w = tid >> 6, kg = lane & 7, nq = lane >> 3; const float sc8 = J.sc8;
; #pragma unroll
;     for (int c = 0; c < 4; ++c) { u32x4 o;
; #pragma unroll
;         for (int d = 0; d < 4; ++d) { int wv = __builtin_amdgcn_cvt_pk_fp8_f32(v[4 * d][c] * sc8, v[4 * d + 1][c] * sc8, 0, false);
;             wv = __builtin_amdgcn_cvt_pk_fp8_f32(v[4 * d + 2][c] * sc8, v[4 * d + 3][c] * sc8, wv, true); o[d] = (unsigned)wv; }
;         *(GAS u32x4*)(J.WT + (size_t)conv_dst_row(J.mode, n0 - J.ncol0 + 32 * w + 4 * nq + c) * J.K + k0 + 16 * kg) = o; }
;     ...
;     auto decode = [&](int it) -> ConvJob {
;         int r = it;
;         if (r < I_IN) return ConvJob{w_in, ws + WS_WIN, D_MODEL, IN_WIDTH, 1, r, 0, IN_WIDTH, 1, 64.f}; r -= I_IN;
;         if (r < I_INF) return ConvJob{w_in, ws + WS_WINF, D_MODEL, IN_WIDTH, 0, r, C_HF, HG_WIDTH, 0, 1.f}; r -= I_INF;
;         if (r < I_HG) return ConvJob{w_hg, ws + WS_WHG, HG_WIDTH, D_MODEL, 0, r, 0, D_MODEL, 0, 1.f}; r -= I_HG;
;         if (r < I_ATT) return ConvJob{w_att, ws + WS_WATT, ATT_OUT, D_MODEL, 0, r, 0, D_MODEL, 0, 1.f}; r -= I_ATT;
;         if (r < I_OUT) return ConvJob{w_out, ws + WS_WOUT, D_MODEL, D_MODEL, 0, r, 0, D_MODEL, 1, 64.f}; r -= I_OUT;
;         const int which = r / (NEXP1 * I_E); r -= which * (NEXP1 * I_E);
;         const int e = r / I_E, ri = r % I_E; const int es = gu8 ? 1 : 2;
;         if (which == 0) return ConvJob{(e < N_EXPERTS) ? w_eg + (size_t)e * D_MODEL * EXPERT_FF : w_sg, ws + (moe8 ? WS_WGU8 : WS_WGU) + (size_t)e * 1024 * D_MODEL * es, D_MODEL, EXPERT_FF, 2, ri, 0, EXPERT_FF, gu8 ? 1 : 0, 64.f};
;         if (which == 1) return ConvJob{(e < N_EXPERTS) ? w_eu + (size_t)e * D_MODEL * EXPERT_FF : w_su, ws + (moe8 ? WS_WGU8 : WS_WGU) + (size_t)e * 1024 * D_MODEL * es, D_MODEL, EXPERT_FF, 3, ri, 0, EXPERT_FF, gu8 ? 1 : 0, 64.f};
;         return ConvJob{(e < N_EXPERTS) ? w_ed + (size_t)e * EXPERT_FF * D_MODEL : w_sd, ws + (moe8 ? WS_WDN8 : WS_WDN) + (size_t)e * D_MODEL * EXPERT_FF, EXPERT_FF, D_MODEL, 0, ri, 0, D_MODEL, 1, 64.f};
.LBB0_1686:
	v_mul_f32_e32 v143, s39, v5
	v_mul_f32_e32 v145, s39, v9
	v_mov_b32_e32 v142, v163
	v_cvt_pk_fp8_f32 v142, v143, v145
	v_mul_f32_e32 v145, s39, v21
	v_mul_f32_e32 v146, s39, v25
	v_mov_b32_e32 v143, v163
	v_cvt_pk_fp8_f32 v143, v145, v146
	v_mul_f32_e32 v141, s39, v13
	v_mul_f32_e32 v144, s39, v17
	v_cvt_pk_fp8_f32 v142, v141, v144 op_sel:[0,0,1]
	v_mul_f32_e32 v141, s39, v29
	v_mul_f32_e32 v144, s39, v33
	v_cvt_pk_fp8_f32 v143, v141, v144 op_sel:[0,0,1]
	v_mul_f32_e32 v145, s39, v37
	v_mul_f32_e32 v147, s39, v41
	v_mov_b32_e32 v144, v163
	v_cvt_pk_fp8_f32 v144, v145, v147
	v_mul_f32_e32 v147, s39, v65
	v_mul_f32_e32 v148, s39, v73
	v_mov_b32_e32 v145, v163
	v_cvt_pk_fp8_f32 v145, v147, v148
	v_mul_f32_e32 v141, s39, v45
	v_mul_f32_e32 v146, s39, v57
	v_cvt_pk_fp8_f32 v144, v141, v146 op_sel:[0,0,1]
	v_mul_f32_e32 v141, s39, v81
	v_mul_f32_e32 v146, s39, v93
	v_cvt_pk_fp8_f32 v145, v141, v146 op_sel:[0,0,1]
	v_ashrrev_i32_e32 v141, 31, v140
	v_mov_b64_e32 v[146:147], s[78:79]
	v_mad_u64_u32 v[146:147], s[38:39], s76, v140, v[146:147]
	v_mul_lo_u32 v140, s77, v140
	v_mul_lo_u32 v141, s76, v141
	v_add3_u32 v147, v140, v147, v141
	v_lshl_add_u64 v[140:141], v[146:147], 0, s[80:81]
	v_lshl_add_u64 v[140:141], v[140:141], 0, v[130:131]
	s_andn2_b64 vcc, exec, s[74:75]
	s_mov_b64 s[74:75], -1
	global_store_dwordx4 v[140:141], v[142:145], off nt
	s_cbranch_vccnz .LBB0_1591
	s_add_i32 s13, s48, s13
	s_cmpk_gt_i32 s13, 0x13ff
	s_cbranch_scc1 .LBB0_1715
	s_add_i32 s2, s13, 0xa0
	s_cmpk_lt_i32 s13, 0x320
	s_cselect_b32 s13, s13, s2
	s_cmpk_lt_i32 s13, 0x320
	s_cbranch_scc1 .LBB0_1713
	s_cmpk_gt_u32 s13, 0x35f
	s_mov_b64 s[78:79], -1
	s_cbranch_scc0 .LBB0_1710
	s_cmpk_gt_u32 s13, 0x39f
	s_cbranch_scc0 .LBB0_1707
	s_cmpk_gt_u32 s13, 0x3bf
	s_cbranch_scc0 .LBB0_1704
	s_cmpk_gt_u32 s13, 0x43f
	s_cbranch_scc0 .LBB0_1701
	s_add_i32 s2, s13, 0xfffffbc0
	s_mul_i32 s38, s2, 0xfc1
	s_lshr_b32 s38, s38, 23
	s_mulk_i32 s38, 0x820
	s_sub_i32 s39, s2, s38
	s_bfe_u32 s44, s39, 0xb0005
	s_cmpk_gt_u32 s2, 0x81f
	s_cbranch_scc0 .LBB0_1698
	s_add_i32 s2, s13, 0xfffff3a0
	s_and_b32 s38, 0xffff, s39
	s_cmpk_lt_u32 s38, 0x800
	v_readlane_b32 s60, v254, 17
	s_cselect_b64 s[76:77], -1, 0
	v_readlane_b32 s61, v254, 18
	s_lshl_b32 s60, s44, 20
	v_writelane_b32 v254, s60, 17
	s_cmpk_gt_u32 s2, 0x81f
	s_nop 0
	v_writelane_b32 v254, s61, 18
	s_cbranch_scc0 .LBB0_1696
	v_readlane_b32 s60, v254, 17
	v_readlane_b32 s61, v254, 18
	s_lshl_b64 s[60:61], s[60:61], 2
	s_add_u32 s2, s11, s60
	s_addc_u32 s38, s24, s61
	s_and_b64 s[60:61], s[76:77], exec
	s_cselect_b32 s75, s38, s43
	s_cselect_b32 s74, s2, s42
	s_mov_b64 s[78:79], 0

; #define GAS __attribute__((address_space(1)))
; __device__ __forceinline__ int conv_dst_row(int mode, int n) {
;     if (mode == 1) { if (n >= C_AQ && n < C_AV) { const int hb = n & ~127, dd = n & 127; return hb + (dd < 64 ? 2 * dd : 2 * (dd - 64) + 1); } return n; }
;     if (mode == 2) return (n >> 7) * 256 + (n & 127);
;     if (mode == 3) return (n >> 7) * 256 + 128 + (n & 127);
;     return n;
; __device__ __forceinline__ void conv8_store(const ConvJob& J, int tid, const f32x4 (&v)[16]) {
;     const int nblk = J.ncols / 256, k0 = 128 * (J.item / nblk), n0 = J.ncol0 + 256 * (J.item % nblk);
;     const int lane = tid & 63, w = tid >> 6, kg = lane & 7, nq = lane >> 3; const float sc8 = J.sc8;
; #pragma unroll
;     for (int c = 0; c < 4; ++c) { u32x4 o;
; #pragma unroll
;         for (int d = 0; d < 4; ++d) { int wv = __builtin_amdgcn_cvt_pk_fp8_f32(v[4 * d][c] * sc8, v[4 * d + 1][c] * sc8, 0, false);
;             wv = __builtin_amdgcn_cvt_pk_fp8_f32(v[4 * d + 2][c] * sc8, v[4 * d + 3][c] * sc8, wv, true); o[d] = (unsigned)wv; }
;         *(GAS u32x4*)(J.WT + (size_t)conv_dst_row(J.mode, n0 - J.ncol0 + 32 * w + 4 * nq + c) * J.K + k0 + 16 * kg) = o; }
.LBB0_1751:
	v_mul_f32_e32 v143, s38, v46
	v_mul_f32_e32 v144, s38, v50
	v_mov_b32_e32 v142, v163
	v_cvt_pk_fp8_f32 v142, v143, v144
	v_mul_f32_e32 v146, s38, v74
	v_mul_f32_e32 v147, s38, v82
	v_mov_b32_e32 v143, v163
	v_cvt_pk_fp8_f32 v143, v146, v147
	v_mul_f32_e32 v144, s38, v58
	v_mul_f32_e32 v145, s38, v66
	v_cvt_pk_fp8_f32 v142, v144, v145 op_sel:[0,0,1]
	v_mul_f32_e32 v144, s38, v86
	v_mul_f32_e32 v145, s38, v94
	v_cvt_pk_fp8_f32 v143, v144, v145 op_sel:[0,0,1]
	v_mul_f32_e32 v145, s38, v98
	v_mul_f32_e32 v146, s38, v102
	v_mov_b32_e32 v144, v163
	v_cvt_pk_fp8_f32 v144, v145, v146
	v_mul_f32_e32 v148, s38, v114
	v_mul_f32_e32 v149, s38, v118
	v_mov_b32_e32 v145, v163
	v_cvt_pk_fp8_f32 v145, v148, v149
	v_mul_f32_e32 v146, s38, v106
	v_mul_f32_e32 v147, s38, v110
	v_cvt_pk_fp8_f32 v144, v146, v147 op_sel:[0,0,1]
	v_mul_f32_e32 v146, s38, v122
	v_mul_f32_e32 v147, s38, v126
	s_add_i32 s44, s44, s39
	v_cvt_pk_fp8_f32 v145, v146, v147 op_sel:[0,0,1]
	v_ashrrev_i32_e32 v148, 31, v141
	v_mov_b64_e32 v[146:147], s[76:77]
	v_add_u32_e32 v140, s44, v136
	s_lshl_b32 s78, s46, 7
	v_mad_u64_u32 v[146:147], s[44:45], s74, v141, v[146:147]
	v_mul_lo_u32 v141, s75, v141
	v_mul_lo_u32 v148, s74, v148
	s_ashr_i32 s79, s78, 31
	v_add3_u32 v147, v141, v147, v148
	v_lshl_add_u64 v[146:147], v[146:147], 0, s[78:79]
	v_lshl_add_u64 v[146:147], v[146:147], 0, v[130:131]
	global_store_dwordx4 v[146:147], v[142:145], off nt
	s_cmp_lt_i32 s13, 2
	s_mov_b64 s[80:81], -1
	v_or_b32_e32 v143, 1, v140
	v_subrev_u32_e32 v142, s39, v143
	s_cbranch_scc1 .LBB0_1757
	s_cmp_gt_i32 s13, 2
	v_lshlrev_b32_e32 v144, 1, v142
	s_cbranch_scc0 .LBB0_1754
	v_and_b32_e32 v141, 0xffffff00, v144
	v_and_b32_e32 v145, 0x7d, v143
	v_or3_b32 v141, v145, v141, s5
	s_mov_b64 s[80:81], 0

; #define GAS __attribute__((address_space(1)))
; __device__ __forceinline__ int conv_dst_row(int mode, int n) {
;     if (mode == 1) { if (n >= C_AQ && n < C_AV) { const int hb = n & ~127, dd = n & 127; return hb + (dd < 64 ? 2 * dd : 2 * (dd - 64) + 1); } return n; }
;     if (mode == 2) return (n >> 7) * 256 + (n & 127);
;     if (mode == 3) return (n >> 7) * 256 + 128 + (n & 127);
;     return n;
; __device__ __forceinline__ void conv8_store(const ConvJob& J, int tid, const f32x4 (&v)[16]) {
;     const int nblk = J.ncols / 256, k0 = 128 * (J.item / nblk), n0 = J.ncol0 + 256 * (J.item % nblk);
;     const int lane = tid & 63, w = tid >> 6, kg = lane & 7, nq = lane >> 3; const float sc8 = J.sc8;
; #pragma unroll
;     for (int c = 0; c < 4; ++c) { u32x4 o;
; #pragma unroll
;         for (int d = 0; d < 4; ++d) { int wv = __builtin_amdgcn_cvt_pk_fp8_f32(v[4 * d][c] * sc8, v[4 * d + 1][c] * sc8, 0, false);
;             wv = __builtin_amdgcn_cvt_pk_fp8_f32(v[4 * d + 2][c] * sc8, v[4 * d + 3][c] * sc8, wv, true); o[d] = (unsigned)wv; }
;         *(GAS u32x4*)(J.WT + (size_t)conv_dst_row(J.mode, n0 - J.ncol0 + 32 * w + 4 * nq + c) * J.K + k0 + 16 * kg) = o; }
.LBB0_1761:
	v_mul_f32_e32 v143, s38, v47
	v_mul_f32_e32 v144, s38, v51
	v_mov_b32_e32 v142, v163
	v_cvt_pk_fp8_f32 v142, v143, v144
	v_mul_f32_e32 v146, s38, v75
	v_mul_f32_e32 v147, s38, v83
	v_mov_b32_e32 v143, v163
	v_cvt_pk_fp8_f32 v143, v146, v147
	v_mul_f32_e32 v144, s38, v59
	v_mul_f32_e32 v145, s38, v67
	v_cvt_pk_fp8_f32 v142, v144, v145 op_sel:[0,0,1]
	v_mul_f32_e32 v144, s38, v87
	v_mul_f32_e32 v145, s38, v95
	v_cvt_pk_fp8_f32 v143, v144, v145 op_sel:[0,0,1]
	v_mul_f32_e32 v145, s38, v99
	v_mul_f32_e32 v146, s38, v103
	v_mov_b32_e32 v144, v163
	v_cvt_pk_fp8_f32 v144, v145, v146
	v_mul_f32_e32 v148, s38, v115
	v_mul_f32_e32 v149, s38, v119
	v_mov_b32_e32 v145, v163
	v_cvt_pk_fp8_f32 v145, v148, v149
	v_mul_f32_e32 v146, s38, v107
	v_mul_f32_e32 v147, s38, v111
	v_cvt_pk_fp8_f32 v144, v146, v147 op_sel:[0,0,1]
	v_mul_f32_e32 v146, s38, v123
	v_mul_f32_e32 v147, s38, v127
	v_cvt_pk_fp8_f32 v145, v146, v147 op_sel:[0,0,1]
	v_ashrrev_i32_e32 v148, 31, v141
	v_mov_b64_e32 v[146:147], s[76:77]
	v_mad_u64_u32 v[146:147], s[44:45], s74, v141, v[146:147]
	v_mul_lo_u32 v141, s75, v141
	v_mul_lo_u32 v148, s74, v148
	v_add3_u32 v147, v141, v147, v148
	v_lshl_add_u64 v[146:147], v[146:147], 0, s[78:79]
	v_lshl_add_u64 v[146:147], v[146:147], 0, v[130:131]
	global_store_dwordx4 v[146:147], v[142:145], off nt
	s_cmp_lt_i32 s13, 2
	s_mov_b64 s[80:81], -1
	v_or_b32_e32 v143, 2, v140
	v_subrev_u32_e32 v142, s39, v143
	s_cbranch_scc1 .LBB0_1767
	s_cmp_gt_i32 s13, 2
	v_lshlrev_b32_e32 v144, 1, v142
	s_cbranch_scc0 .LBB0_1764
	v_and_b32_e32 v141, 0xffffff00, v144
	v_and_b32_e32 v145, 0x7e, v143
	v_or3_b32 v141, v145, v141, s5
	s_mov_b64 s[80:81], 0

; #define GAS __attribute__((address_space(1)))
; __device__ __forceinline__ int conv_dst_row(int mode, int n) {
;     if (mode == 1) { if (n >= C_AQ && n < C_AV) { const int hb = n & ~127, dd = n & 127; return hb + (dd < 64 ? 2 * dd : 2 * (dd - 64) + 1); } return n; }
;     if (mode == 2) return (n >> 7) * 256 + (n & 127);
;     if (mode == 3) return (n >> 7) * 256 + 128 + (n & 127);
;     return n;
; __device__ __forceinline__ void conv8_store(const ConvJob& J, int tid, const f32x4 (&v)[16]) {
;     const int nblk = J.ncols / 256, k0 = 128 * (J.item / nblk), n0 = J.ncol0 + 256 * (J.item % nblk);
;     const int lane = tid & 63, w = tid >> 6, kg = lane & 7, nq = lane >> 3; const float sc8 = J.sc8;
; #pragma unroll
;     for (int c = 0; c < 4; ++c) { u32x4 o;
; #pragma unroll
;         for (int d = 0; d < 4; ++d) { int wv = __builtin_amdgcn_cvt_pk_fp8_f32(v[4 * d][c] * sc8, v[4 * d + 1][c] * sc8, 0, false);
;             wv = __builtin_amdgcn_cvt_pk_fp8_f32(v[4 * d + 2][c] * sc8, v[4 * d + 3][c] * sc8, wv, true); o[d] = (unsigned)wv; }
;         *(GAS u32x4*)(J.WT + (size_t)conv_dst_row(J.mode, n0 - J.ncol0 + 32 * w + 4 * nq + c) * J.K + k0 + 16 * kg) = o; }
.LBB0_1771:
	v_mul_f32_e32 v143, s38, v48
	v_mul_f32_e32 v144, s38, v52
	v_mov_b32_e32 v142, v163
	v_cvt_pk_fp8_f32 v142, v143, v144
	v_mul_f32_e32 v146, s38, v76
	v_mul_f32_e32 v147, s38, v84
	v_mov_b32_e32 v143, v163
	v_cvt_pk_fp8_f32 v143, v146, v147
	v_mul_f32_e32 v144, s38, v60
	v_mul_f32_e32 v145, s38, v68
	v_cvt_pk_fp8_f32 v142, v144, v145 op_sel:[0,0,1]
	v_mul_f32_e32 v144, s38, v88
	v_mul_f32_e32 v145, s38, v96
	v_cvt_pk_fp8_f32 v143, v144, v145 op_sel:[0,0,1]
	v_mul_f32_e32 v145, s38, v100
	v_mul_f32_e32 v146, s38, v104
	v_mov_b32_e32 v144, v163
	v_cvt_pk_fp8_f32 v144, v145, v146
	v_mul_f32_e32 v148, s38, v116
	v_mul_f32_e32 v149, s38, v120
	v_mov_b32_e32 v145, v163
	v_cvt_pk_fp8_f32 v145, v148, v149
	v_mul_f32_e32 v146, s38, v108
	v_mul_f32_e32 v147, s38, v112
	v_cvt_pk_fp8_f32 v144, v146, v147 op_sel:[0,0,1]
	v_mul_f32_e32 v146, s38, v124
	v_mul_f32_e32 v147, s38, v128
	v_cvt_pk_fp8_f32 v145, v146, v147 op_sel:[0,0,1]
	v_ashrrev_i32_e32 v148, 31, v141
	v_mov_b64_e32 v[146:147], s[76:77]
	v_mad_u64_u32 v[146:147], s[44:45], s74, v141, v[146:147]
	v_mul_lo_u32 v141, s75, v141
	v_mul_lo_u32 v148, s74, v148
	v_add3_u32 v147, v141, v147, v148
	v_lshl_add_u64 v[146:147], v[146:147], 0, s[78:79]
	v_lshl_add_u64 v[146:147], v[146:147], 0, v[130:131]
	global_store_dwordx4 v[146:147], v[142:145], off nt
	s_cmp_lt_i32 s13, 2
	s_mov_b64 s[80:81], -1
	v_or_b32_e32 v142, 3, v140
	v_subrev_u32_e32 v141, s39, v142
	s_cbranch_scc1 .LBB0_1777
	s_cmp_gt_i32 s13, 2
	v_lshlrev_b32_e32 v143, 1, v141
	s_cbranch_scc0 .LBB0_1774
	v_and_b32_e32 v140, 0xffffff00, v143
	v_and_b32_e32 v144, 0x7f, v142
	v_or3_b32 v140, v144, v140, s5
	s_mov_b64 s[80:81], 0

; #define GAS __attribute__((address_space(1)))
; #define LAS __attribute__((address_space(3)))
; __device__ __forceinline__ void conv_load(const ConvJob& J, int tid, f32x4 (&v)[16]) {
;     const int nblk = J.ncols / 256, k0 = 128 * (J.item / nblk), n0 = J.ncol0 + 256 * (J.item % nblk);
;     {
; #pragma unroll
;         for (int ii = 0; ii < 16; ++ii) { const int idx = tid + 512 * ii, k = idx >> 6, c4 = idx & 63; v[ii] = *(const GAS f32x4*)(J.W + (size_t)(k0 + k) * J.N + n0 + 4 * c4); }
;     }
; }
; __device__ __forceinline__ void conv_to_lds(const ConvJob& J, int tid, const f32x4 (&v)[16], LAS float* T) {
; #pragma unroll
;     for (int ii = 0; ii < 16; ++ii) { const int idx = tid + 512 * ii, k = idx >> 6, c4 = idx & 63; const int g = J.f8 ? ((k >> 4) & 7) : ((k >> 3) & 15);
;         *(LAS f32x4*)(T + k * 256 + 4 * (c4 ^ g)) = v[ii]; }
; }
.LBB0_1797:
	v_cvt_f32_ubyte0_e32 v114, s12
	v_rcp_iflag_f32_e32 v114, v114
	s_sub_i32 s24, 0, s12
	s_abs_i32 s13, s10
	s_ashr_i32 s2, s10, 31
	v_mul_f32_e32 v114, 0x4f7ffffe, v114
	v_cvt_u32_f32_e32 v114, v114
	v_xor_b32_e32 v113, v113, v23
	v_xor_b32_e32 v112, v112, v23
	v_xor_b32_e32 v111, v111, v23
	v_readfirstlane_b32 s25, v114
	s_mul_i32 s24, s24, s25
	s_mul_hi_u32 s24, s25, s24
	s_add_i32 s25, s25, s24
	s_mul_hi_u32 s24, s13, s25
	s_mul_i32 s25, s24, s12
	s_sub_i32 s13, s13, s25
	s_add_i32 s33, s24, 1
	s_sub_i32 s25, s13, s12
	s_cmp_ge_u32 s13, s12
	s_cselect_b32 s24, s33, s24
	s_cselect_b32 s13, s25, s13
	s_add_i32 s25, s24, 1
	s_cmp_ge_u32 s13, s12
	s_cselect_b32 s13, s25, s24
	s_xor_b32 s13, s13, s2
	s_sub_i32 s2, s13, s2
	s_lshl_b32 s74, s2, 7
	s_mul_i32 s2, s2, s12
	s_sub_i32 s2, s10, s2
	s_lshl_b32 s10, s2, 8
	s_add_i32 s12, s10, s11
	s_ashr_i32 s13, s12, 31
	v_add_u32_e32 v114, s74, v3
	v_add_u32_e32 v116, s74, v8
	v_add_u32_e32 v122, s74, v9
	v_add_u32_e32 v124, s74, v10
	v_add_u32_e32 v130, s74, v11
	v_add_u32_e32 v132, s74, v12
	v_add_u32_e32 v138, s74, v13
	v_add_u32_e32 v140, s74, v14
	v_add_u32_e32 v146, s74, v15
	v_add_u32_e32 v148, s74, v16
	v_add_u32_e32 v154, s74, v17
	v_add_u32_e32 v156, s74, v18
	v_add_u32_e32 v164, s74, v19
	v_add_u32_e32 v166, s74, v20
	v_add_u32_e32 v172, s74, v21
	v_add_u32_e32 v176, s74, v22
	v_mad_i64_i32 v[114:115], s[24:25], s82, v114, 0
	s_lshl_b64 s[84:85], s[12:13], 2
	v_mad_i64_i32 v[116:117], s[12:13], s82, v116, 0
	v_mad_i64_i32 v[122:123], s[12:13], s82, v122, 0
	v_mad_i64_i32 v[124:125], s[12:13], s82, v124, 0
	v_mad_i64_i32 v[130:131], s[12:13], s82, v130, 0
	v_mad_i64_i32 v[132:133], s[12:13], s82, v132, 0
	v_mad_i64_i32 v[138:139], s[12:13], s82, v138, 0
	v_mad_i64_i32 v[140:141], s[12:13], s82, v140, 0
	v_mad_i64_i32 v[146:147], s[12:13], s82, v146, 0
	v_mad_i64_i32 v[148:149], s[12:13], s82, v148, 0
	v_mad_i64_i32 v[154:155], s[12:13], s82, v154, 0
	v_mad_i64_i32 v[156:157], s[12:13], s82, v156, 0
	v_mad_i64_i32 v[164:165], s[12:13], s82, v164, 0
	v_mad_i64_i32 v[166:167], s[12:13], s82, v166, 0
	v_mad_i64_i32 v[172:173], s[12:13], s82, v172, 0
	v_mad_i64_i32 v[176:177], s[12:13], s82, v176, 0
	v_lshl_add_u64 v[114:115], v[114:115], 2, s[80:81]
	v_lshl_add_u64 v[116:117], v[116:117], 2, s[80:81]
	v_lshl_add_u64 v[122:123], v[122:123], 2, s[80:81]
	v_lshl_add_u64 v[124:125], v[124:125], 2, s[80:81]
	v_lshl_add_u64 v[130:131], v[130:131], 2, s[80:81]
	v_lshl_add_u64 v[132:133], v[132:133], 2, s[80:81]
	v_lshl_add_u64 v[138:139], v[138:139], 2, s[80:81]
	v_lshl_add_u64 v[140:141], v[140:141], 2, s[80:81]
	v_lshl_add_u64 v[146:147], v[146:147], 2, s[80:81]
	v_lshl_add_u64 v[148:149], v[148:149], 2, s[80:81]
	v_lshl_add_u64 v[154:155], v[154:155], 2, s[80:81]
	v_lshl_add_u64 v[156:157], v[156:157], 2, s[80:81]
	v_lshl_add_u64 v[164:165], v[164:165], 2, s[80:81]
	v_lshl_add_u64 v[166:167], v[166:167], 2, s[80:81]
	v_lshl_add_u64 v[172:173], v[172:173], 2, s[80:81]
	v_lshl_add_u64 v[176:177], v[176:177], 2, s[80:81]
	v_lshl_add_u64 v[114:115], v[114:115], 0, s[84:85]
	v_lshl_add_u64 v[116:117], v[116:117], 0, s[84:85]
	v_lshl_add_u64 v[122:123], v[122:123], 0, s[84:85]
	v_lshl_add_u64 v[124:125], v[124:125], 0, s[84:85]
	v_lshl_add_u64 v[130:131], v[130:131], 0, s[84:85]
	v_lshl_add_u64 v[132:133], v[132:133], 0, s[84:85]
	v_lshl_add_u64 v[138:139], v[138:139], 0, s[84:85]
	v_lshl_add_u64 v[140:141], v[140:141], 0, s[84:85]
	v_lshl_add_u64 v[146:147], v[146:147], 0, s[84:85]
	v_lshl_add_u64 v[148:149], v[148:149], 0, s[84:85]
	v_lshl_add_u64 v[154:155], v[154:155], 0, s[84:85]
	v_lshl_add_u64 v[156:157], v[156:157], 0, s[84:85]
	v_lshl_add_u64 v[164:165], v[164:165], 0, s[84:85]
	v_lshl_add_u64 v[166:167], v[166:167], 0, s[84:85]
	v_lshl_add_u64 v[172:173], v[172:173], 0, s[84:85]
	v_lshl_add_u64 v[176:177], v[176:177], 0, s[84:85]
	v_lshl_add_u64 v[114:115], v[114:115], 0, v[162:163]
	v_lshl_add_u64 v[118:119], v[116:117], 0, v[162:163]
	v_lshl_add_u64 v[122:123], v[122:123], 0, v[162:163]
	v_lshl_add_u64 v[126:127], v[124:125], 0, v[162:163]
	v_lshl_add_u64 v[130:131], v[130:131], 0, v[162:163]
	v_lshl_add_u64 v[134:135], v[132:133], 0, v[162:163]
	v_lshl_add_u64 v[138:139], v[138:139], 0, v[162:163]
	v_lshl_add_u64 v[142:143], v[140:141], 0, v[162:163]
	v_lshl_add_u64 v[146:147], v[146:147], 0, v[162:163]
	v_lshl_add_u64 v[150:151], v[148:149], 0, v[162:163]
	v_lshl_add_u64 v[154:155], v[154:155], 0, v[162:163]
	v_lshl_add_u64 v[158:159], v[156:157], 0, v[162:163]
	v_lshl_add_u64 v[164:165], v[164:165], 0, v[162:163]
	v_lshl_add_u64 v[168:169], v[166:167], 0, v[162:163]
	v_lshl_add_u64 v[172:173], v[172:173], 0, v[162:163]
	v_lshl_add_u64 v[176:177], v[176:177], 0, v[162:163]
	global_load_dwordx4 v[114:117], v[114:115], off nt
	s_nop 0
	global_load_dwordx4 v[118:121], v[118:119], off nt
	s_nop 0
	global_load_dwordx4 v[122:125], v[122:123], off nt
	s_nop 0
	global_load_dwordx4 v[126:129], v[126:127], off nt
	s_nop 0
	global_load_dwordx4 v[130:133], v[130:131], off nt
	s_nop 0
	global_load_dwordx4 v[134:137], v[134:135], off nt
	s_nop 0
	global_load_dwordx4 v[138:141], v[138:139], off nt
	s_nop 0
	global_load_dwordx4 v[142:145], v[142:143], off nt
	s_nop 0
	global_load_dwordx4 v[146:149], v[146:147], off nt
	s_nop 0
	global_load_dwordx4 v[150:153], v[150:151], off nt
	s_nop 0
	global_load_dwordx4 v[154:157], v[154:155], off nt
	s_nop 0
	global_load_dwordx4 v[158:161], v[158:159], off nt
	s_nop 0
	global_load_dwordx4 v[164:167], v[164:165], off nt
	s_nop 0
	global_load_dwordx4 v[168:171], v[168:169], off nt
	v_xor_b32_e32 v110, v110, v23
	global_load_dwordx4 v[172:175], v[172:173], off nt
	v_xor_b32_e32 v109, v109, v23
	global_load_dwordx4 v[176:179], v[176:177], off nt
	v_xor_b32_e32 v108, v108, v23
	v_xor_b32_e32 v107, v107, v23
	v_xor_b32_e32 v106, v106, v23
	v_xor_b32_e32 v105, v105, v23
	v_xor_b32_e32 v104, v104, v23
	v_xor_b32_e32 v103, v103, v23
	v_xor_b32_e32 v102, v102, v23
	v_xor_b32_e32 v101, v101, v23
	v_xor_b32_e32 v100, v100, v23
	v_xor_b32_e32 v7, v7, v23
	v_xor_b32_e32 v6, v6, v23
	v_lshl_add_u32 v113, v113, 4, v26
	v_lshl_add_u32 v112, v112, 4, v29
	v_lshl_add_u32 v111, v111, 4, v32
	v_lshl_add_u32 v110, v110, 4, v35
	v_lshl_add_u32 v109, v109, 4, v38
	v_lshl_add_u32 v108, v108, 4, v41
	v_lshl_add_u32 v107, v107, 4, v44
	v_lshl_add_u32 v106, v106, 4, v47
	v_lshl_add_u32 v105, v105, 4, v50
	v_lshl_add_u32 v104, v104, 4, v53
	v_lshl_add_u32 v103, v103, 4, v56
	v_lshl_add_u32 v102, v102, 4, v59
	v_lshl_add_u32 v101, v101, 4, v62
	v_lshl_add_u32 v100, v100, 4, v65
	v_lshl_add_u32 v7, v7, 4, v68
	v_lshl_add_u32 v6, v6, 4, v71
	s_ashr_i32 s75, s74, 31
	s_mov_b64 s[80:81], -1
	s_and_b64 vcc, exec, s[78:79]
	s_waitcnt vmcnt(15)
; #define GAS __attribute__((address_space(1)))
; #define LAS __attribute__((address_space(3)))
; __device__ __forceinline__ unsigned cvt_pk_bf16(float lo, float hi) { unsigned r; asm volatile("v_cvt_pk_bf16_f32 %0, %1, %2" : "=v"(r) : "v"(lo), "v"(hi)); return r; }
; __device__ __forceinline__ void conv_to_lds(const ConvJob& J, int tid, const f32x4 (&v)[16], LAS float* T) {
;     ...
;     for (int ii = 0; ii < 16; ++ii) { const int idx = tid + 512 * ii, k = idx >> 6, c4 = idx & 63; const int g = J.f8 ? ((k >> 4) & 7) : ((k >> 3) & 15);
;         *(LAS f32x4*)(T + k * 256 + 4 * (c4 ^ g)) = v[ii]; }
; }
; __device__ __forceinline__ void conv_from_lds(const ConvJob& J, int tid, const LAS float* T) {
;     const int nblk = J.ncols / 256, k0 = 128 * (J.item / nblk), n0 = J.ncol0 + 256 * (J.item % nblk);
;     const int lane = tid & 63, w = tid >> 6, j = lane & 3;
;     if (J.f8) {
;         const int c = (lane >> 2) & 7; const float sc8 = J.sc8;
; #pragma unroll
;         for (int it = 0; it < 4; ++it) { const int c4n = w * 8 + it * 2 + (lane >> 5), n = 4 * c4n + j; const LAS float* base = T + 4 * (c4n ^ c) + j; u32x4 o;
; #pragma unroll
;             for (int d = 0; d < 4; ++d) { const int kk = 16 * c + 4 * d;
;                 int wv = __builtin_amdgcn_cvt_pk_fp8_f32(base[(kk + 0) * 256] * sc8, base[(kk + 1) * 256] * sc8, 0, false);
;                 wv = __builtin_amdgcn_cvt_pk_fp8_f32(base[(kk + 2) * 256] * sc8, base[(kk + 3) * 256] * sc8, wv, true); o[d] = (unsigned)wv; }
;             *(GAS u32x4*)(J.WT + (size_t)conv_dst_row(J.mode, n0 - J.ncol0 + n) * J.K + k0 + 16 * c) = o; }
;     } else {
;         const int c = ((lane >> 2) & 7) + 8 * (lane >> 5);
; #pragma unroll
;         for (int it = 0; it < 8; ++it) { const int c4n = w * 8 + it, n = 4 * c4n + j; const LAS float* base = T + 4 * (c4n ^ c) + j + (8 * c) * 256;
;             u32x4 o; o.x = cvt_pk_bf16(base[0 * 256], base[1 * 256]); o.y = cvt_pk_bf16(base[2 * 256], base[3 * 256]); o.z = cvt_pk_bf16(base[4 * 256], base[5 * 256]); o.w = cvt_pk_bf16(base[6 * 256], base[7 * 256]);
;             *(GAS u32x4*)(J.WT + ((size_t)conv_dst_row(J.mode, n0 - J.ncol0 + n) * J.K + k0 + 8 * c) * 2) = o; }
	ds_write_b128 v113, v[114:117]
	s_waitcnt vmcnt(14)
	ds_write_b128 v112, v[118:121]
	s_waitcnt vmcnt(13)
	ds_write_b128 v111, v[122:125]
	s_waitcnt vmcnt(12)
	ds_write_b128 v110, v[126:129]
	s_waitcnt vmcnt(11)
	ds_write_b128 v109, v[130:133]
	s_waitcnt vmcnt(10)
	ds_write_b128 v108, v[134:137]
	s_waitcnt vmcnt(9)
	ds_write_b128 v107, v[138:141]
	s_waitcnt vmcnt(8)
	ds_write_b128 v106, v[142:145]
	s_waitcnt vmcnt(7)
	ds_write_b128 v105, v[146:149]
	s_waitcnt vmcnt(6)
	ds_write_b128 v104, v[150:153]
	s_waitcnt vmcnt(5)
	ds_write_b128 v103, v[154:157]
	s_waitcnt vmcnt(4)
	ds_write_b128 v102, v[158:161]
	s_waitcnt vmcnt(3)
	ds_write_b128 v101, v[164:167]
	s_waitcnt vmcnt(2)
	ds_write_b128 v100, v[168:171]
	s_waitcnt vmcnt(1)
	ds_write_b128 v7, v[172:175]
	s_waitcnt vmcnt(0)
	ds_write_b128 v6, v[176:179]
	s_waitcnt lgkmcnt(0)
	s_barrier
	s_cbranch_vccz .LBB0_1799
	ds_read2st64_b32 v[100:101], v88 offset1:4
	s_waitcnt lgkmcnt(0)
	v_cvt_pk_bf16_f32 v100, v100, v101
	ds_read2st64_b32 v[102:103], v88 offset0:8 offset1:12
	s_waitcnt lgkmcnt(0)
	v_cvt_pk_bf16_f32 v101, v102, v103
	ds_read2st64_b32 v[102:103], v88 offset0:16 offset1:20
	s_waitcnt lgkmcnt(0)
	v_cvt_pk_bf16_f32 v102, v102, v103
	ds_read2st64_b32 v[104:105], v88 offset0:24 offset1:28
	v_add_u32_e32 v106, s10, v72
	v_mov_b32_e32 v7, s75
	v_or_b32_e32 v6, s74, v2
	s_waitcnt lgkmcnt(0)
	v_cvt_pk_bf16_f32 v103, v104, v105
	v_ashrrev_i32_e32 v104, 31, v106
	v_mul_lo_u32 v107, s72, v104
	v_mad_u64_u32 v[104:105], s[12:13], s72, v106, v[6:7]
	v_mul_lo_u32 v106, s73, v106
	v_add3_u32 v105, v106, v105, v107
	v_lshl_add_u64 v[104:105], v[104:105], 1, s[76:77]
	global_store_dwordx4 v[104:105], v[100:103], off nt
	ds_read2st64_b32 v[100:101], v89 offset1:4
	v_add_u32_e32 v106, s10, v73
	s_waitcnt lgkmcnt(0)
	v_cvt_pk_bf16_f32 v100, v100, v101
	ds_read2st64_b32 v[102:103], v89 offset0:8 offset1:12
	s_waitcnt lgkmcnt(0)
	v_cvt_pk_bf16_f32 v101, v102, v103
	ds_read2st64_b32 v[102:103], v89 offset0:16 offset1:20
	s_waitcnt lgkmcnt(0)
	v_cvt_pk_bf16_f32 v102, v102, v103
	ds_read2st64_b32 v[104:105], v89 offset0:24 offset1:28
	s_waitcnt lgkmcnt(0)
	v_cvt_pk_bf16_f32 v103, v104, v105
	v_ashrrev_i32_e32 v104, 31, v106
	v_mul_lo_u32 v107, s72, v104
	v_mad_u64_u32 v[104:105], s[12:13], s72, v106, v[6:7]
	v_mul_lo_u32 v106, s73, v106
	v_add3_u32 v105, v106, v105, v107
	v_lshl_add_u64 v[104:105], v[104:105], 1, s[76:77]
	global_store_dwordx4 v[104:105], v[100:103], off nt
	ds_read2st64_b32 v[100:101], v90 offset1:4
	v_add_u32_e32 v106, s10, v74
	s_waitcnt lgkmcnt(0)
	v_cvt_pk_bf16_f32 v100, v100, v101
	ds_read2st64_b32 v[102:103], v90 offset0:8 offset1:12
	s_waitcnt lgkmcnt(0)
	v_cvt_pk_bf16_f32 v101, v102, v103
	ds_read2st64_b32 v[102:103], v90 offset0:16 offset1:20
	s_waitcnt lgkmcnt(0)
	v_cvt_pk_bf16_f32 v102, v102, v103
	ds_read2st64_b32 v[104:105], v90 offset0:24 offset1:28
	s_waitcnt lgkmcnt(0)
	v_cvt_pk_bf16_f32 v103, v104, v105
	v_ashrrev_i32_e32 v104, 31, v106
	v_mul_lo_u32 v107, s72, v104
	v_mad_u64_u32 v[104:105], s[12:13], s72, v106, v[6:7]
	v_mul_lo_u32 v106, s73, v106
	v_add3_u32 v105, v106, v105, v107
	v_lshl_add_u64 v[104:105], v[104:105], 1, s[76:77]
	global_store_dwordx4 v[104:105], v[100:103], off nt
	ds_read2st64_b32 v[100:101], v91 offset1:4
	v_add_u32_e32 v106, s10, v75
	s_waitcnt lgkmcnt(0)
	v_cvt_pk_bf16_f32 v100, v100, v101
	ds_read2st64_b32 v[102:103], v91 offset0:8 offset1:12
	s_waitcnt lgkmcnt(0)
	v_cvt_pk_bf16_f32 v101, v102, v103
	ds_read2st64_b32 v[102:103], v91 offset0:16 offset1:20
	s_waitcnt lgkmcnt(0)
	v_cvt_pk_bf16_f32 v102, v102, v103
	ds_read2st64_b32 v[104:105], v91 offset0:24 offset1:28
	s_waitcnt lgkmcnt(0)
	v_cvt_pk_bf16_f32 v103, v104, v105
	v_ashrrev_i32_e32 v104, 31, v106
	v_mul_lo_u32 v107, s72, v104
	v_mad_u64_u32 v[104:105], s[12:13], s72, v106, v[6:7]
	v_mul_lo_u32 v106, s73, v106
	v_add3_u32 v105, v106, v105, v107
	v_lshl_add_u64 v[104:105], v[104:105], 1, s[76:77]
	global_store_dwordx4 v[104:105], v[100:103], off nt
	ds_read2st64_b32 v[100:101], v92 offset1:4
	v_add_u32_e32 v106, s10, v76
	s_waitcnt lgkmcnt(0)
	v_cvt_pk_bf16_f32 v100, v100, v101
	ds_read2st64_b32 v[102:103], v92 offset0:8 offset1:12
	s_waitcnt lgkmcnt(0)
	v_cvt_pk_bf16_f32 v101, v102, v103
	ds_read2st64_b32 v[102:103], v92 offset0:16 offset1:20
	s_waitcnt lgkmcnt(0)
	v_cvt_pk_bf16_f32 v102, v102, v103
	ds_read2st64_b32 v[104:105], v92 offset0:24 offset1:28
	s_waitcnt lgkmcnt(0)
	v_cvt_pk_bf16_f32 v103, v104, v105
	v_ashrrev_i32_e32 v104, 31, v106
	v_mul_lo_u32 v107, s72, v104
	v_mad_u64_u32 v[104:105], s[12:13], s72, v106, v[6:7]
	v_mul_lo_u32 v106, s73, v106
	v_add3_u32 v105, v106, v105, v107
	v_lshl_add_u64 v[104:105], v[104:105], 1, s[76:77]
	global_store_dwordx4 v[104:105], v[100:103], off nt
	ds_read2st64_b32 v[100:101], v93 offset1:4
	v_add_u32_e32 v106, s10, v77
	s_waitcnt lgkmcnt(0)
	v_cvt_pk_bf16_f32 v100, v100, v101
	ds_read2st64_b32 v[102:103], v93 offset0:8 offset1:12
	s_waitcnt lgkmcnt(0)
	v_cvt_pk_bf16_f32 v101, v102, v103
	ds_read2st64_b32 v[102:103], v93 offset0:16 offset1:20
	s_waitcnt lgkmcnt(0)
	v_cvt_pk_bf16_f32 v102, v102, v103
	ds_read2st64_b32 v[104:105], v93 offset0:24 offset1:28
	s_waitcnt lgkmcnt(0)
	v_cvt_pk_bf16_f32 v103, v104, v105
	v_ashrrev_i32_e32 v104, 31, v106
	v_mul_lo_u32 v107, s72, v104
	v_mad_u64_u32 v[104:105], s[12:13], s72, v106, v[6:7]
	v_mul_lo_u32 v106, s73, v106
	v_add3_u32 v105, v106, v105, v107
	v_lshl_add_u64 v[104:105], v[104:105], 1, s[76:77]
	global_store_dwordx4 v[104:105], v[100:103], off nt
	ds_read2st64_b32 v[100:101], v94 offset1:4
	v_add_u32_e32 v106, s10, v78
	s_waitcnt lgkmcnt(0)
	v_cvt_pk_bf16_f32 v100, v100, v101
	ds_read2st64_b32 v[102:103], v94 offset0:8 offset1:12
	s_waitcnt lgkmcnt(0)
	v_cvt_pk_bf16_f32 v101, v102, v103
	ds_read2st64_b32 v[102:103], v94 offset0:16 offset1:20
	s_waitcnt lgkmcnt(0)
	v_cvt_pk_bf16_f32 v102, v102, v103
	ds_read2st64_b32 v[104:105], v94 offset0:24 offset1:28
	s_waitcnt lgkmcnt(0)
	v_cvt_pk_bf16_f32 v103, v104, v105
	v_ashrrev_i32_e32 v104, 31, v106
	v_mul_lo_u32 v107, s72, v104
	v_mad_u64_u32 v[104:105], s[12:13], s72, v106, v[6:7]
	v_mul_lo_u32 v106, s73, v106
	v_add3_u32 v105, v106, v105, v107
	v_lshl_add_u64 v[104:105], v[104:105], 1, s[76:77]
	global_store_dwordx4 v[104:105], v[100:103], off nt
	ds_read2st64_b32 v[100:101], v95 offset1:4
	s_mov_b64 s[80:81], 0
	s_waitcnt lgkmcnt(0)
	v_cvt_pk_bf16_f32 v100, v100, v101
	ds_read2st64_b32 v[102:103], v95 offset0:8 offset1:12
	s_waitcnt lgkmcnt(0)
	v_cvt_pk_bf16_f32 v101, v102, v103
	ds_read2st64_b32 v[102:103], v95 offset0:16 offset1:20
	s_waitcnt lgkmcnt(0)
	v_cvt_pk_bf16_f32 v102, v102, v103
	ds_read2st64_b32 v[104:105], v95 offset0:24 offset1:28
	s_waitcnt lgkmcnt(0)
	v_cvt_pk_bf16_f32 v103, v104, v105
	v_add_u32_e32 v104, s10, v79
	v_ashrrev_i32_e32 v105, 31, v104
	v_mul_lo_u32 v105, s72, v105
	v_mad_u64_u32 v[6:7], s[12:13], s72, v104, v[6:7]
	v_mul_lo_u32 v104, s73, v104
	v_add3_u32 v7, v104, v7, v105
	v_lshl_add_u64 v[6:7], v[6:7], 1, s[76:77]
	global_store_dwordx4 v[6:7], v[100:103], off nt
; #define GAS __attribute__((address_space(1)))
; #define LAS __attribute__((address_space(3)))
; __device__ __forceinline__ int conv_dst_row(int mode, int n) {
;     if (mode == 1) { if (n >= C_AQ && n < C_AV) { const int hb = n & ~127, dd = n & 127; return hb + (dd < 64 ? 2 * dd : 2 * (dd - 64) + 1); } return n; }
;     if (mode == 2) return (n >> 7) * 256 + (n & 127);
;     if (mode == 3) return (n >> 7) * 256 + 128 + (n & 127);
;     return n;
; __device__ __forceinline__ void conv_from_lds(const ConvJob& J, int tid, const LAS float* T) {
;     ...
;     if (J.f8) {
;         const int c = (lane >> 2) & 7; const float sc8 = J.sc8;
; #pragma unroll
;         for (int it = 0; it < 4; ++it) { const int c4n = w * 8 + it * 2 + (lane >> 5), n = 4 * c4n + j; const LAS float* base = T + 4 * (c4n ^ c) + j; u32x4 o;
; #pragma unroll
;             for (int d = 0; d < 4; ++d) { const int kk = 16 * c + 4 * d;
;                 int wv = __builtin_amdgcn_cvt_pk_fp8_f32(base[(kk + 0) * 256] * sc8, base[(kk + 1) * 256] * sc8, 0, false);
;                 wv = __builtin_amdgcn_cvt_pk_fp8_f32(base[(kk + 2) * 256] * sc8, base[(kk + 3) * 256] * sc8, wv, true); o[d] = (unsigned)wv; }
;             *(GAS u32x4*)(J.WT + (size_t)conv_dst_row(J.mode, n0 - J.ncol0 + n) * J.K + k0 + 16 * c) = o; }
.LBB0_1799:
	s_andn2_b64 vcc, exec, s[80:81]
	s_cbranch_vccnz .LBB0_1786
	ds_read2st64_b32 v[6:7], v96 offset1:4
	v_mov_b32_e32 v100, v163
	v_mov_b32_e32 v101, v163
	v_mov_b32_e32 v102, v163
	v_mov_b32_e32 v103, v163
	s_waitcnt lgkmcnt(0)
	v_mul_f32_e32 v6, s9, v6
	v_mul_f32_e32 v7, s9, v7
	v_cvt_pk_fp8_f32 v100, v6, v7
	ds_read2st64_b32 v[6:7], v96 offset0:8 offset1:12
	s_waitcnt lgkmcnt(0)
	v_mul_f32_e32 v6, s9, v6
	v_mul_f32_e32 v7, s9, v7
	v_cvt_pk_fp8_f32 v100, v6, v7 op_sel:[0,0,1]
	ds_read2st64_b32 v[6:7], v96 offset0:16 offset1:20
	s_waitcnt lgkmcnt(0)
	v_mul_f32_e32 v6, s9, v6
	v_mul_f32_e32 v7, s9, v7
	v_cvt_pk_fp8_f32 v101, v6, v7
	ds_read2st64_b32 v[6:7], v96 offset0:24 offset1:28
	s_waitcnt lgkmcnt(0)
	v_mul_f32_e32 v6, s9, v6
	v_mul_f32_e32 v7, s9, v7
	v_cvt_pk_fp8_f32 v101, v6, v7 op_sel:[0,0,1]
	ds_read2st64_b32 v[6:7], v96 offset0:32 offset1:36
	s_waitcnt lgkmcnt(0)
	v_mul_f32_e32 v6, s9, v6
	v_mul_f32_e32 v7, s9, v7
	v_cvt_pk_fp8_f32 v102, v6, v7
	ds_read2st64_b32 v[6:7], v96 offset0:40 offset1:44
	s_waitcnt lgkmcnt(0)
	v_mul_f32_e32 v6, s9, v6
	v_mul_f32_e32 v7, s9, v7
	v_cvt_pk_fp8_f32 v102, v6, v7 op_sel:[0,0,1]
	ds_read2st64_b32 v[6:7], v96 offset0:48 offset1:52
	s_waitcnt lgkmcnt(0)
	v_mul_f32_e32 v6, s9, v6
	v_mul_f32_e32 v7, s9, v7
	v_cvt_pk_fp8_f32 v103, v6, v7
	ds_read2st64_b32 v[6:7], v96 offset0:56 offset1:60
	s_waitcnt lgkmcnt(0)
	v_mul_f32_e32 v6, s9, v6
	v_mul_f32_e32 v7, s9, v7
	v_cvt_pk_fp8_f32 v103, v6, v7 op_sel:[0,0,1]
	v_add_u32_e32 v6, s10, v80
	v_add_u32_e32 v7, 0xfffff000, v6
	v_cmp_gt_u32_e32 vcc, s4, v7
	v_and_b32_e32 v7, 0x1f80, v6
	v_add_u32_e32 v7, v7, v81
	v_cndmask_b32_e32 v104, v6, v7, vcc
	v_ashrrev_i32_e32 v6, 31, v104
	v_mul_lo_u32 v106, s72, v6
	v_mov_b64_e32 v[6:7], s[76:77]
	v_mul_lo_u32 v107, s73, v104
	v_mad_u64_u32 v[104:105], s[12:13], s72, v104, v[6:7]
	v_add3_u32 v105, v107, v105, v106
	v_lshl_add_u64 v[104:105], v[104:105], 0, s[74:75]
	v_lshl_add_u64 v[104:105], v[104:105], 0, v[4:5]
	global_store_dwordx4 v[104:105], v[100:103], off nt
	ds_read2st64_b32 v[100:101], v97 offset1:4
	s_waitcnt lgkmcnt(0)
	v_mul_f32_e32 v102, s9, v100
	v_mul_f32_e32 v101, s9, v101
	v_mov_b32_e32 v100, v163
	v_cvt_pk_fp8_f32 v100, v102, v101
	ds_read2st64_b32 v[102:103], v97 offset0:8 offset1:12
	s_waitcnt lgkmcnt(0)
	v_mul_f32_e32 v101, s9, v102
	v_mul_f32_e32 v102, s9, v103
	v_cvt_pk_fp8_f32 v100, v101, v102 op_sel:[0,0,1]
	ds_read2st64_b32 v[102:103], v97 offset0:16 offset1:20
	v_mov_b32_e32 v101, v163
	s_waitcnt lgkmcnt(0)
	v_mul_f32_e32 v102, s9, v102
	v_mul_f32_e32 v103, s9, v103
	v_cvt_pk_fp8_f32 v101, v102, v103
	ds_read2st64_b32 v[102:103], v97 offset0:24 offset1:28
	s_waitcnt lgkmcnt(0)
	v_mul_f32_e32 v102, s9, v102
	v_mul_f32_e32 v103, s9, v103
	v_cvt_pk_fp8_f32 v101, v102, v103 op_sel:[0,0,1]
	ds_read2st64_b32 v[102:103], v97 offset0:32 offset1:36
	s_waitcnt lgkmcnt(0)
	v_mul_f32_e32 v104, s9, v102
	v_mul_f32_e32 v103, s9, v103
	v_mov_b32_e32 v102, v163
	v_cvt_pk_fp8_f32 v102, v104, v103
	ds_read2st64_b32 v[104:105], v97 offset0:40 offset1:44
	s_waitcnt lgkmcnt(0)
	v_mul_f32_e32 v103, s9, v104
	v_mul_f32_e32 v104, s9, v105
	v_cvt_pk_fp8_f32 v102, v103, v104 op_sel:[0,0,1]
	ds_read2st64_b32 v[104:105], v97 offset0:48 offset1:52
	v_mov_b32_e32 v103, v163
	s_waitcnt lgkmcnt(0)
	v_mul_f32_e32 v104, s9, v104
	v_mul_f32_e32 v105, s9, v105
	v_cvt_pk_fp8_f32 v103, v104, v105
	ds_read2st64_b32 v[104:105], v97 offset0:56 offset1:60
	s_waitcnt lgkmcnt(0)
	v_mul_f32_e32 v104, s9, v104
	v_mul_f32_e32 v105, s9, v105
	v_cvt_pk_fp8_f32 v103, v104, v105 op_sel:[0,0,1]
	v_add_u32_e32 v104, s10, v82
	v_add_u32_e32 v105, 0xfffff000, v104
	v_cmp_gt_u32_e32 vcc, s4, v105
	v_and_b32_e32 v105, 0x1f80, v104
	v_add_u32_e32 v105, v105, v83
	v_cndmask_b32_e32 v104, v104, v105, vcc
	v_ashrrev_i32_e32 v105, 31, v104
	v_mul_lo_u32 v106, s72, v105
	v_mul_lo_u32 v107, s73, v104
	v_mad_u64_u32 v[104:105], s[12:13], s72, v104, v[6:7]
	v_add3_u32 v105, v107, v105, v106
	v_lshl_add_u64 v[104:105], v[104:105], 0, s[74:75]
	v_lshl_add_u64 v[104:105], v[104:105], 0, v[4:5]
	global_store_dwordx4 v[104:105], v[100:103], off nt
	ds_read2st64_b32 v[100:101], v98 offset1:4
	s_waitcnt lgkmcnt(0)
; #define GAS __attribute__((address_space(1)))
; #define LAS __attribute__((address_space(3)))
; __device__ __forceinline__ int conv_dst_row(int mode, int n) {
;     if (mode == 1) { if (n >= C_AQ && n < C_AV) { const int hb = n & ~127, dd = n & 127; return hb + (dd < 64 ? 2 * dd : 2 * (dd - 64) + 1); } return n; }
;     if (mode == 2) return (n >> 7) * 256 + (n & 127);
;     if (mode == 3) return (n >> 7) * 256 + 128 + (n & 127);
;     return n;
; __device__ __forceinline__ void conv_from_lds(const ConvJob& J, int tid, const LAS float* T) {
;     ...
;         for (int it = 0; it < 4; ++it) { const int c4n = w * 8 + it * 2 + (lane >> 5), n = 4 * c4n + j; const LAS float* base = T + 4 * (c4n ^ c) + j; u32x4 o;
; #pragma unroll
;             for (int d = 0; d < 4; ++d) { const int kk = 16 * c + 4 * d;
;                 int wv = __builtin_amdgcn_cvt_pk_fp8_f32(base[(kk + 0) * 256] * sc8, base[(kk + 1) * 256] * sc8, 0, false);
;                 wv = __builtin_amdgcn_cvt_pk_fp8_f32(base[(kk + 2) * 256] * sc8, base[(kk + 3) * 256] * sc8, wv, true); o[d] = (unsigned)wv; }
;             *(GAS u32x4*)(J.WT + (size_t)conv_dst_row(J.mode, n0 - J.ncol0 + n) * J.K + k0 + 16 * c) = o; }
	v_mul_f32_e32 v102, s9, v100
	v_mul_f32_e32 v101, s9, v101
	v_mov_b32_e32 v100, v163
	v_cvt_pk_fp8_f32 v100, v102, v101
	ds_read2st64_b32 v[102:103], v98 offset0:8 offset1:12
	s_waitcnt lgkmcnt(0)
	v_mul_f32_e32 v101, s9, v102
	v_mul_f32_e32 v102, s9, v103
	v_cvt_pk_fp8_f32 v100, v101, v102 op_sel:[0,0,1]
	ds_read2st64_b32 v[102:103], v98 offset0:16 offset1:20
	v_mov_b32_e32 v101, v163
	s_waitcnt lgkmcnt(0)
	v_mul_f32_e32 v102, s9, v102
	v_mul_f32_e32 v103, s9, v103
	v_cvt_pk_fp8_f32 v101, v102, v103
	ds_read2st64_b32 v[102:103], v98 offset0:24 offset1:28
	s_waitcnt lgkmcnt(0)
	v_mul_f32_e32 v102, s9, v102
	v_mul_f32_e32 v103, s9, v103
	v_cvt_pk_fp8_f32 v101, v102, v103 op_sel:[0,0,1]
	ds_read2st64_b32 v[102:103], v98 offset0:32 offset1:36
	s_waitcnt lgkmcnt(0)
	v_mul_f32_e32 v104, s9, v102
	v_mul_f32_e32 v103, s9, v103
	v_mov_b32_e32 v102, v163
	v_cvt_pk_fp8_f32 v102, v104, v103
	ds_read2st64_b32 v[104:105], v98 offset0:40 offset1:44
	s_waitcnt lgkmcnt(0)
	v_mul_f32_e32 v103, s9, v104
	v_mul_f32_e32 v104, s9, v105
	v_cvt_pk_fp8_f32 v102, v103, v104 op_sel:[0,0,1]
	ds_read2st64_b32 v[104:105], v98 offset0:48 offset1:52
	v_mov_b32_e32 v103, v163
	s_waitcnt lgkmcnt(0)
	v_mul_f32_e32 v104, s9, v104
	v_mul_f32_e32 v105, s9, v105
	v_cvt_pk_fp8_f32 v103, v104, v105
	ds_read2st64_b32 v[104:105], v98 offset0:56 offset1:60
	s_waitcnt lgkmcnt(0)
	v_mul_f32_e32 v104, s9, v104
	v_mul_f32_e32 v105, s9, v105
	v_cvt_pk_fp8_f32 v103, v104, v105 op_sel:[0,0,1]
	v_add_u32_e32 v104, s10, v84
	v_add_u32_e32 v105, 0xfffff000, v104
	v_cmp_gt_u32_e32 vcc, s4, v105
	v_and_b32_e32 v105, 0x1f80, v104
	v_add_u32_e32 v105, v105, v85
	v_cndmask_b32_e32 v104, v104, v105, vcc
	v_ashrrev_i32_e32 v105, 31, v104
	v_mul_lo_u32 v106, s72, v105
	v_mul_lo_u32 v107, s73, v104
	v_mad_u64_u32 v[104:105], s[12:13], s72, v104, v[6:7]
	v_add3_u32 v105, v107, v105, v106
	v_lshl_add_u64 v[104:105], v[104:105], 0, s[74:75]
	v_lshl_add_u64 v[104:105], v[104:105], 0, v[4:5]
	global_store_dwordx4 v[104:105], v[100:103], off nt
	ds_read2st64_b32 v[100:101], v99 offset1:4
	s_waitcnt lgkmcnt(0)
	v_mul_f32_e32 v102, s9, v100
	v_mul_f32_e32 v101, s9, v101
	v_mov_b32_e32 v100, v163
	v_cvt_pk_fp8_f32 v100, v102, v101
	ds_read2st64_b32 v[102:103], v99 offset0:8 offset1:12
	s_waitcnt lgkmcnt(0)
	v_mul_f32_e32 v101, s9, v102
	v_mul_f32_e32 v102, s9, v103
	v_cvt_pk_fp8_f32 v100, v101, v102 op_sel:[0,0,1]
	ds_read2st64_b32 v[102:103], v99 offset0:16 offset1:20
	v_mov_b32_e32 v101, v163
	s_waitcnt lgkmcnt(0)
	v_mul_f32_e32 v102, s9, v102
	v_mul_f32_e32 v103, s9, v103
	v_cvt_pk_fp8_f32 v101, v102, v103
	ds_read2st64_b32 v[102:103], v99 offset0:24 offset1:28
	s_waitcnt lgkmcnt(0)
	v_mul_f32_e32 v102, s9, v102
	v_mul_f32_e32 v103, s9, v103
	v_cvt_pk_fp8_f32 v101, v102, v103 op_sel:[0,0,1]
	ds_read2st64_b32 v[102:103], v99 offset0:32 offset1:36
	s_waitcnt lgkmcnt(0)
	v_mul_f32_e32 v104, s9, v102
	v_mul_f32_e32 v103, s9, v103
	v_mov_b32_e32 v102, v163
	v_cvt_pk_fp8_f32 v102, v104, v103
	ds_read2st64_b32 v[104:105], v99 offset0:40 offset1:44
	s_waitcnt lgkmcnt(0)
	v_mul_f32_e32 v103, s9, v104
	v_mul_f32_e32 v104, s9, v105
	v_cvt_pk_fp8_f32 v102, v103, v104 op_sel:[0,0,1]
	ds_read2st64_b32 v[104:105], v99 offset0:48 offset1:52
	v_mov_b32_e32 v103, v163
	s_waitcnt lgkmcnt(0)
	v_mul_f32_e32 v104, s9, v104
	v_mul_f32_e32 v105, s9, v105
	v_cvt_pk_fp8_f32 v103, v104, v105
	ds_read2st64_b32 v[104:105], v99 offset0:56 offset1:60
	s_waitcnt lgkmcnt(0)
	v_mul_f32_e32 v104, s9, v104
	v_mul_f32_e32 v105, s9, v105
	v_cvt_pk_fp8_f32 v103, v104, v105 op_sel:[0,0,1]
	v_add_u32_e32 v104, s10, v86
	v_add_u32_e32 v105, 0xfffff000, v104
	v_cmp_gt_u32_e32 vcc, s4, v105
	v_and_b32_e32 v105, 0x1f80, v104
	v_add_u32_e32 v105, v105, v87
	v_cndmask_b32_e32 v104, v104, v105, vcc
	v_ashrrev_i32_e32 v105, 31, v104
	v_mul_lo_u32 v105, s72, v105
	v_mul_lo_u32 v106, s73, v104
	v_mad_u64_u32 v[6:7], s[10:11], s72, v104, v[6:7]
	v_add3_u32 v7, v106, v7, v105
	v_lshl_add_u64 v[6:7], v[6:7], 0, s[74:75]
	v_lshl_add_u64 v[6:7], v[6:7], 0, v[4:5]
	global_store_dwordx4 v[6:7], v[100:103], off nt
	s_branch .LBB0_1786

; #define GAS __attribute__((address_space(1)))
; __device__ __forceinline__ void conv8_store(const ConvJob& J, int tid, const f32x4 (&v)[16]) {
;     const int nblk = J.ncols / 256, k0 = 128 * (J.item / nblk), n0 = J.ncol0 + 256 * (J.item % nblk);
;     const int lane = tid & 63, w = tid >> 6, kg = lane & 7, nq = lane >> 3; const float sc8 = J.sc8;
; #pragma unroll
;     for (int c = 0; c < 4; ++c) { u32x4 o;
; #pragma unroll
;         for (int d = 0; d < 4; ++d) { int wv = __builtin_amdgcn_cvt_pk_fp8_f32(v[4 * d][c] * sc8, v[4 * d + 1][c] * sc8, 0, false);
;             wv = __builtin_amdgcn_cvt_pk_fp8_f32(v[4 * d + 2][c] * sc8, v[4 * d + 3][c] * sc8, wv, true); o[d] = (unsigned)wv; }
;         *(GAS u32x4*)(J.WT + (size_t)conv_dst_row(J.mode, n0 - J.ncol0 + 32 * w + 4 * nq + c) * J.K + k0 + 16 * kg) = o; }
.LBB0_1803:
	v_mul_f32_e32 v7, s56, v29
	v_mul_f32_e32 v8, s56, v33
	v_mov_b32_e32 v6, v71
	v_cvt_pk_fp8_f32 v6, v7, v8
	v_mul_f32_e32 v8, s56, v45
	v_mul_f32_e32 v10, s56, v49
	v_mov_b32_e32 v7, v71
	v_cvt_pk_fp8_f32 v7, v8, v10
	v_mul_f32_e32 v9, s56, v9
	v_mul_f32_e32 v10, s56, v21
	v_mov_b32_e32 v8, v71
	v_cvt_pk_fp8_f32 v8, v9, v10
	v_mul_f32_e32 v10, s56, v13
	v_mul_f32_e32 v11, s56, v25
	v_mov_b32_e32 v9, v71
	v_mul_f32_e32 v3, s56, v61
	v_mul_f32_e32 v4, s56, v65
	v_cvt_pk_fp8_f32 v9, v10, v11
	v_cvt_pk_fp8_f32 v6, v3, v4 op_sel:[0,0,1]
	v_mul_f32_e32 v3, s56, v37
	v_mul_f32_e32 v4, s56, v41
	v_cvt_pk_fp8_f32 v7, v3, v4 op_sel:[0,0,1]
	v_mul_f32_e32 v3, s56, v53
	v_mul_f32_e32 v4, s56, v57
	v_cvt_pk_fp8_f32 v8, v3, v4 op_sel:[0,0,1]
	v_mul_f32_e32 v3, s56, v5
	v_mul_f32_e32 v4, s56, v17
	v_cvt_pk_fp8_f32 v9, v3, v4 op_sel:[0,0,1]
	v_ashrrev_i32_e32 v3, 31, v2
	v_mov_b64_e32 v[4:5], s[36:37]
	v_mad_u64_u32 v[4:5], s[36:37], s34, v2, v[4:5]
	v_mul_lo_u32 v2, s35, v2
	v_mul_lo_u32 v3, s34, v3
	v_add3_u32 v5, v2, v5, v3
	v_lshl_add_u64 v[2:3], v[4:5], 0, s[38:39]
	v_lshl_add_u64 v[2:3], v[2:3], 0, v[66:67]
	s_mov_b64 s[34:35], 0
	global_store_dwordx4 v[2:3], v[6:9], off nt

; #define GAS __attribute__((address_space(1)))
; __device__ __forceinline__ int conv_dst_row(int mode, int n) {
;     if (mode == 1) { if (n >= C_AQ && n < C_AV) { const int hb = n & ~127, dd = n & 127; return hb + (dd < 64 ? 2 * dd : 2 * (dd - 64) + 1); } return n; }
;     if (mode == 2) return (n >> 7) * 256 + (n & 127);
;     if (mode == 3) return (n >> 7) * 256 + 128 + (n & 127);
;     return n;
; __device__ __forceinline__ void conv8_store(const ConvJob& J, int tid, const f32x4 (&v)[16]) {
;     const int nblk = J.ncols / 256, k0 = 128 * (J.item / nblk), n0 = J.ncol0 + 256 * (J.item % nblk);
;     const int lane = tid & 63, w = tid >> 6, kg = lane & 7, nq = lane >> 3; const float sc8 = J.sc8;
; #pragma unroll
;     for (int c = 0; c < 4; ++c) { u32x4 o;
; #pragma unroll
;         for (int d = 0; d < 4; ++d) { int wv = __builtin_amdgcn_cvt_pk_fp8_f32(v[4 * d][c] * sc8, v[4 * d + 1][c] * sc8, 0, false);
;             wv = __builtin_amdgcn_cvt_pk_fp8_f32(v[4 * d + 2][c] * sc8, v[4 * d + 3][c] * sc8, wv, true); o[d] = (unsigned)wv; }
;         *(GAS u32x4*)(J.WT + (size_t)conv_dst_row(J.mode, n0 - J.ncol0 + 32 * w + 4 * nq + c) * J.K + k0 + 16 * kg) = o; }
.LBB0_1846:
	s_waitcnt vmcnt(7)
	v_mul_f32_e32 v6, s56, v6
	s_waitcnt vmcnt(6)
	v_mul_f32_e32 v18, s56, v18
	v_mov_b32_e32 v80, v71
	v_mul_f32_e32 v26, s56, v26
	v_mul_f32_e32 v30, s56, v30
	v_mov_b32_e32 v78, v71
	v_cvt_pk_fp8_f32 v80, v6, v18
	s_waitcnt vmcnt(3)
	v_mul_f32_e32 v10, s56, v10
	s_waitcnt vmcnt(2)
	v_mul_f32_e32 v22, s56, v22
	v_mov_b32_e32 v81, v71
	v_cvt_pk_fp8_f32 v78, v26, v30
	v_mul_f32_e32 v42, s56, v42
	v_mul_f32_e32 v46, s56, v46
	v_mov_b32_e32 v79, v71
	v_cvt_pk_fp8_f32 v81, v10, v22
	v_cvt_pk_fp8_f32 v79, v42, v46
	v_mul_f32_e32 v6, s56, v50
	v_mul_f32_e32 v18, s56, v54
	v_mul_f32_e32 v26, s56, v58
	v_mul_f32_e32 v30, s56, v62
	v_cvt_pk_fp8_f32 v80, v6, v18 op_sel:[0,0,1]
	s_waitcnt vmcnt(1)
	v_mul_f32_e32 v2, s56, v2
	s_waitcnt vmcnt(0)
	v_mul_f32_e32 v6, s56, v14
	v_cvt_pk_fp8_f32 v78, v26, v30 op_sel:[0,0,1]
	v_mul_f32_e32 v26, s56, v34
	v_mul_f32_e32 v30, s56, v38
	v_cvt_pk_fp8_f32 v81, v2, v6 op_sel:[0,0,1]
	v_ashrrev_i32_e32 v2, 31, v77
	v_mov_b64_e32 v[82:83], s[36:37]
	v_cvt_pk_fp8_f32 v79, v26, v30 op_sel:[0,0,1]
	v_mad_u64_u32 v[82:83], s[40:41], s34, v77, v[82:83]
	v_mul_lo_u32 v6, s35, v77
	v_mul_lo_u32 v2, s34, v2
	v_add_u32_e32 v76, s44, v1
	v_add3_u32 v83, v6, v83, v2
	v_lshl_add_u64 v[82:83], v[82:83], 0, s[38:39]
	v_or_b32_e32 v10, 1, v76
	v_lshl_add_u64 v[82:83], v[82:83], 0, v[66:67]
	v_subrev_u32_e32 v6, s57, v10
	s_cmp_lt_i32 s30, 2
	s_mov_b64 s[40:41], -1
	global_store_dwordx4 v[82:83], v[78:81], off nt
	s_cbranch_scc1 .LBB0_1852
	s_cmp_gt_i32 s30, 2
	v_lshlrev_b32_e32 v14, 1, v6
	s_cbranch_scc0 .LBB0_1849
	v_and_b32_e32 v2, 0xffffff00, v14
	v_and_b32_e32 v18, 0x7d, v10
	v_or3_b32 v2, v18, v2, s48
	s_mov_b64 s[40:41], 0

; #define GAS __attribute__((address_space(1)))
; __device__ __forceinline__ int conv_dst_row(int mode, int n) {
;     if (mode == 1) { if (n >= C_AQ && n < C_AV) { const int hb = n & ~127, dd = n & 127; return hb + (dd < 64 ? 2 * dd : 2 * (dd - 64) + 1); } return n; }
;     if (mode == 2) return (n >> 7) * 256 + (n & 127);
;     if (mode == 3) return (n >> 7) * 256 + 128 + (n & 127);
;     return n;
; __device__ __forceinline__ void conv8_store(const ConvJob& J, int tid, const f32x4 (&v)[16]) {
;     const int nblk = J.ncols / 256, k0 = 128 * (J.item / nblk), n0 = J.ncol0 + 256 * (J.item % nblk);
;     const int lane = tid & 63, w = tid >> 6, kg = lane & 7, nq = lane >> 3; const float sc8 = J.sc8;
; #pragma unroll
;     for (int c = 0; c < 4; ++c) { u32x4 o;
; #pragma unroll
;         for (int d = 0; d < 4; ++d) { int wv = __builtin_amdgcn_cvt_pk_fp8_f32(v[4 * d][c] * sc8, v[4 * d + 1][c] * sc8, 0, false);
;             wv = __builtin_amdgcn_cvt_pk_fp8_f32(v[4 * d + 2][c] * sc8, v[4 * d + 3][c] * sc8, wv, true); o[d] = (unsigned)wv; }
;         *(GAS u32x4*)(J.WT + (size_t)conv_dst_row(J.mode, n0 - J.ncol0 + 32 * w + 4 * nq + c) * J.K + k0 + 16 * kg) = o; }
.LBB0_1856:
	v_mul_f32_e32 v6, s56, v27
	v_mul_f32_e32 v10, s56, v31
	v_mov_b32_e32 v78, v71
	v_cvt_pk_fp8_f32 v78, v6, v10
	v_mul_f32_e32 v14, s56, v43
	v_mul_f32_e32 v18, s56, v47
	v_mov_b32_e32 v79, v71
	v_cvt_pk_fp8_f32 v79, v14, v18
	v_mul_f32_e32 v6, s56, v59
	v_mul_f32_e32 v10, s56, v63
	v_cvt_pk_fp8_f32 v78, v6, v10 op_sel:[0,0,1]
	v_mul_f32_e32 v6, s56, v35
	v_mul_f32_e32 v10, s56, v39
	v_cvt_pk_fp8_f32 v79, v6, v10 op_sel:[0,0,1]
	v_mul_f32_e32 v6, s56, v7
	v_mul_f32_e32 v7, s56, v19
	v_mov_b32_e32 v80, v71
	v_cvt_pk_fp8_f32 v80, v6, v7
	v_mul_f32_e32 v10, s56, v11
	v_mul_f32_e32 v11, s56, v23
	v_mov_b32_e32 v81, v71
	v_cvt_pk_fp8_f32 v81, v10, v11
	v_mul_f32_e32 v6, s56, v51
	v_mul_f32_e32 v7, s56, v55
	v_cvt_pk_fp8_f32 v80, v6, v7 op_sel:[0,0,1]
	v_mul_f32_e32 v3, s56, v3
	v_mul_f32_e32 v6, s56, v15
	v_cvt_pk_fp8_f32 v81, v3, v6 op_sel:[0,0,1]
	v_ashrrev_i32_e32 v3, 31, v2
	v_mov_b64_e32 v[6:7], s[36:37]
	v_mad_u64_u32 v[6:7], s[40:41], s34, v2, v[6:7]
	v_mul_lo_u32 v2, s35, v2
	v_mul_lo_u32 v3, s34, v3
	v_add3_u32 v7, v2, v7, v3
	v_lshl_add_u64 v[2:3], v[6:7], 0, s[38:39]
	v_lshl_add_u64 v[2:3], v[2:3], 0, v[66:67]
	v_or_b32_e32 v6, 2, v76
	global_store_dwordx4 v[2:3], v[78:81], off nt
	v_subrev_u32_e32 v3, s57, v6
	s_cmp_lt_i32 s30, 2
	s_mov_b64 s[40:41], -1
	s_cbranch_scc1 .LBB0_1862
	s_cmp_gt_i32 s30, 2
	v_lshlrev_b32_e32 v7, 1, v3
	s_cbranch_scc0 .LBB0_1859
	v_and_b32_e32 v2, 0xffffff00, v7
	v_and_b32_e32 v10, 0x7e, v6
	v_or3_b32 v2, v10, v2, s48
	s_mov_b64 s[40:41], 0

; #define GAS __attribute__((address_space(1)))
; __device__ __forceinline__ int conv_dst_row(int mode, int n) {
;     if (mode == 1) { if (n >= C_AQ && n < C_AV) { const int hb = n & ~127, dd = n & 127; return hb + (dd < 64 ? 2 * dd : 2 * (dd - 64) + 1); } return n; }
;     if (mode == 2) return (n >> 7) * 256 + (n & 127);
;     if (mode == 3) return (n >> 7) * 256 + 128 + (n & 127);
;     return n;
; __device__ __forceinline__ void conv8_store(const ConvJob& J, int tid, const f32x4 (&v)[16]) {
;     const int nblk = J.ncols / 256, k0 = 128 * (J.item / nblk), n0 = J.ncol0 + 256 * (J.item % nblk);
;     const int lane = tid & 63, w = tid >> 6, kg = lane & 7, nq = lane >> 3; const float sc8 = J.sc8;
; #pragma unroll
;     for (int c = 0; c < 4; ++c) { u32x4 o;
; #pragma unroll
;         for (int d = 0; d < 4; ++d) { int wv = __builtin_amdgcn_cvt_pk_fp8_f32(v[4 * d][c] * sc8, v[4 * d + 1][c] * sc8, 0, false);
;             wv = __builtin_amdgcn_cvt_pk_fp8_f32(v[4 * d + 2][c] * sc8, v[4 * d + 3][c] * sc8, wv, true); o[d] = (unsigned)wv; }
;         *(GAS u32x4*)(J.WT + (size_t)conv_dst_row(J.mode, n0 - J.ncol0 + 32 * w + 4 * nq + c) * J.K + k0 + 16 * kg) = o; }
.LBB0_1866:
	v_mul_f32_e32 v3, s56, v28
	v_mul_f32_e32 v6, s56, v32
	v_mov_b32_e32 v78, v71
	v_cvt_pk_fp8_f32 v78, v3, v6
	v_mul_f32_e32 v7, s56, v44
	v_mul_f32_e32 v10, s56, v48
	v_mov_b32_e32 v79, v71
	v_cvt_pk_fp8_f32 v79, v7, v10
	v_mul_f32_e32 v3, s56, v60
	v_mul_f32_e32 v6, s56, v64
	v_cvt_pk_fp8_f32 v78, v3, v6 op_sel:[0,0,1]
	v_mul_f32_e32 v3, s56, v36
	v_mul_f32_e32 v6, s56, v40
	v_cvt_pk_fp8_f32 v79, v3, v6 op_sel:[0,0,1]
	v_mul_f32_e32 v3, s56, v8
	v_mul_f32_e32 v6, s56, v20
	v_mov_b32_e32 v80, v71
	v_cvt_pk_fp8_f32 v80, v3, v6
	v_mul_f32_e32 v7, s56, v12
	v_mul_f32_e32 v8, s56, v24
	v_mov_b32_e32 v81, v71
	v_cvt_pk_fp8_f32 v81, v7, v8
	v_mul_f32_e32 v3, s56, v52
	v_mul_f32_e32 v6, s56, v56
	v_cvt_pk_fp8_f32 v80, v3, v6 op_sel:[0,0,1]
	v_mul_f32_e32 v3, s56, v4
	v_mul_f32_e32 v4, s56, v16
	v_cvt_pk_fp8_f32 v81, v3, v4 op_sel:[0,0,1]
	v_ashrrev_i32_e32 v3, 31, v2
	v_mov_b64_e32 v[6:7], s[36:37]
	v_mad_u64_u32 v[6:7], s[40:41], s34, v2, v[6:7]
	v_mul_lo_u32 v2, s35, v2
	v_mul_lo_u32 v3, s34, v3
	v_add3_u32 v7, v2, v7, v3
	v_lshl_add_u64 v[2:3], v[6:7], 0, s[38:39]
	v_lshl_add_u64 v[2:3], v[2:3], 0, v[66:67]
	v_or_b32_e32 v4, 3, v76
	global_store_dwordx4 v[2:3], v[78:81], off nt
	v_subrev_u32_e32 v3, s57, v4
	s_cmp_lt_i32 s30, 2
	s_mov_b64 s[40:41], -1
	s_cbranch_scc1 .LBB0_1872
	s_cmp_gt_i32 s30, 2
	v_lshlrev_b32_e32 v6, 1, v3
	s_cbranch_scc0 .LBB0_1869
	v_and_b32_e32 v2, 0xffffff00, v6
	v_and_b32_e32 v7, 0x7f, v4
	v_or3_b32 v2, v7, v2, s48
	s_mov_b64 s[40:41], 0
